# speedup vs baseline: 1.0271x; 1.0271x over previous
_Z11attn_kernelPKDF16_S0_PDF16_:
	s_load_dwordx4 s[4:7], s[0:1], 0x0
	s_load_dwordx2 s[8:9], s[0:1], 0x10
	s_lshr_b32 s1, s2, 3
	s_lshr_b32 s10, s2, 7
	s_and_b32 s0, s2, 4
	s_and_b32 s1, s1, 8
	s_and_b32 s20, s2, 3
	s_lshl_b32 s30, s10, 4
	s_or_b32 s22, s1, s0
	s_or_b32 s0, s30, s20
	s_or_b32 s14, s0, s22
	s_or_b32 s0, s20, 16
	s_sub_i32 s0, s0, s30
	s_mov_b32 s15, 0
	s_or_b32 s0, s0, s22
	s_bfe_u32 s24, s2, 0x30003
	s_ashr_i32 s1, s0, 31
	s_lshl_b64 s[2:3], s[14:15], 18
	s_waitcnt lgkmcnt(0)
	s_add_u32 s2, s4, s2
	s_addc_u32 s3, s5, s3
	s_lshl_b64 s[0:1], s[0:1], 18
	s_add_u32 s11, s4, s0
	s_addc_u32 s12, s5, s1
	s_add_u32 s13, s6, s0
	v_readfirstlane_b32 s16, v0
	s_addc_u32 s18, s7, s1
	s_lshl_b32 s0, s24, 2
	s_lshr_b32 s1, s16, 7
	s_add_i32 s14, s1, s0
	s_lshr_b32 s23, s16, 6
	s_lshl_b64 s[0:1], s[14:15], 13
	s_add_u32 s0, s2, s0
	v_and_b32_e32 v189, 31, v0
	s_addc_u32 s1, s3, s1
	s_lshl_b32 s21, s23, 5
	v_and_or_b32 v1, s21, 32, v189
	v_lshlrev_b32_e32 v186, 4, v1
	v_mov_b32_e32 v187, 0
	s_lshl_b32 s14, s23, 9
	v_lshl_add_u64 v[2:3], s[0:1], 0, v[186:187]
	s_and_b32 s0, s16, 0x3fffffc0
	s_lshl_b64 s[16:17], s[14:15], 1
	v_and_b32_e32 v188, 63, v0
	s_add_u32 s2, s11, s16
	s_addc_u32 s3, s12, s17
	v_lshlrev_b32_e32 v186, 4, v188
	v_lshl_add_u64 v[44:45], s[2:3], 0, v[186:187]
	s_add_u32 s2, s13, s16
	s_addc_u32 s3, s18, s17
	s_lshl_b32 s25, s23, 10
	s_cmp_lg_u32 0, -1
	s_cselect_b32 s1, 0, 0
	v_bfe_u32 v46, v0, 5, 1
	s_add_i32 s25, s25, s1
	s_mov_b32 s1, m0
	s_mov_b32 m0, s25
	s_nop 0
	global_load_lds_dwordx4 v[44:45], off
	s_mov_b32 m0, s1
	v_lshl_add_u64 v[34:35], s[2:3], 0, v[186:187]
	s_add_i32 s26, s25, 0x6000
	v_lshlrev_b32_e32 v4, 10, v46
	s_mov_b32 s1, m0
	s_mov_b32 m0, s26
	s_nop 0
	global_load_lds_dwordx4 v[34:35], off
	s_mov_b32 m0, s1
	s_mov_b64 s[18:19], 0x2000
	v_mov_b32_e32 v5, v187
	v_lshl_add_u64 v[6:7], v[44:45], 0, s[18:19]
	s_add_i32 s1, s25, 0x2000
	s_mov_b32 s2, m0
	s_mov_b32 m0, s1
	s_nop 0
	global_load_lds_dwordx4 v[6:7], off
	s_mov_b32 m0, s2
	v_lshl_add_u64 v[2:3], v[2:3], 0, v[4:5]
	global_load_dwordx4 v[136:139], v[2:3], off
	global_load_dwordx4 v[128:131], v[2:3], off offset:2048
	s_movk_i32 s1, 0x1000
	v_add_co_u32_e32 v2, vcc, s1, v2
	v_lshlrev_b32_e32 v1, 4, v189
	s_nop 0
	v_addc_co_u32_e32 v3, vcc, 0, v3, vcc
	global_load_dwordx4 v[120:123], v[2:3], off
	global_load_dwordx4 v[112:115], v[2:3], off offset:2048
	v_add3_u32 v195, 0, v4, v1
	v_mov_b32_e32 v2, v187
	v_mov_b32_e32 v3, v187
	v_mov_b32_e32 v4, v187
	v_mov_b32_e32 v6, v187
	v_mov_b32_e32 v7, v187
	v_mov_b32_e32 v8, v187
	v_mov_b32_e32 v9, v187
	v_mov_b32_e32 v10, v187
	v_mov_b32_e32 v11, v187
	v_mov_b32_e32 v12, v187
	v_mov_b32_e32 v13, v187
	v_mov_b32_e32 v14, v187
	v_mov_b32_e32 v15, v187
	v_mov_b32_e32 v16, v187
	v_mov_b32_e32 v17, v187
	s_mov_b64 s[2:3], 0x4000
	v_lshl_add_u64 v[18:19], v[44:45], 0, s[2:3]
	s_add_i32 s1, s25, 0x4000
	s_mov_b32 s11, m0
	s_mov_b32 m0, s1
	s_nop 0
	global_load_lds_dwordx4 v[18:19], off
	s_mov_b32 m0, s11
	v_lshl_add_u64 v[18:19], v[34:35], 0, s[18:19]
	s_add_i32 s1, s25, 0x8000
	s_mov_b32 s11, m0
	s_mov_b32 m0, s1
	s_nop 0
	global_load_lds_dwordx4 v[18:19], off
	s_mov_b32 m0, s11
	s_waitcnt vmcnt(4) lgkmcnt(0)
	s_barrier
	ds_read_b128 v[36:39], v195
	ds_read_b128 v[40:43], v195 offset:512
	v_lshlrev_b32_e32 v190, 3, v0
	s_mov_b64 s[12:13], 0x6000
	s_or_b32 s14, s22, s20
	s_sub_i32 s14, s14, s30
	s_add_i32 s34, s14, 16
	s_lshl_b32 s0, s0, 2
	s_ashr_i32 s35, s34, 31
	s_lshl_b64 s[34:35], s[34:35], 18
	s_mov_b32 s27, -1
	s_waitcnt vmcnt(3) lgkmcnt(1)
	v_mfma_f32_32x32x16_f16 v[18:33], v[36:39], v[136:139], v[2:17]
	s_movk_i32 s28, 0x6000
	s_movk_i32 s31, 0x2000
	s_movk_i32 s29, 0x4000
	v_lshlrev_b32_e32 v191, 9, v46
	v_lshlrev_b32_e32 v193, 4, v46
	v_lshl_add_u64 v[180:181], v[34:35], 0, s[12:13]
	s_waitcnt lgkmcnt(0)
	v_mfma_f32_32x32x16_f16 v[2:17], v[40:43], v[136:139], v[2:17]
	ds_read_b128 v[36:39], v195 offset:2048
	ds_read_b128 v[40:43], v195 offset:2560
	s_waitcnt vmcnt(2) lgkmcnt(1)
	v_mfma_f32_32x32x16_f16 v[18:33], v[36:39], v[128:131], v[18:33]
	s_waitcnt lgkmcnt(0)
	v_mfma_f32_32x32x16_f16 v[2:17], v[40:43], v[128:131], v[2:17]
	ds_read_b128 v[36:39], v195 offset:4096
	ds_read_b128 v[40:43], v195 offset:4608
	s_waitcnt vmcnt(1) lgkmcnt(1)
	v_mfma_f32_32x32x16_f16 v[18:33], v[36:39], v[120:123], v[18:33]
	s_waitcnt lgkmcnt(0)
	v_mfma_f32_32x32x16_f16 v[2:17], v[40:43], v[120:123], v[2:17]
	ds_read_b128 v[36:39], v195 offset:6144
	ds_read_b128 v[40:43], v195 offset:6656
	s_waitcnt vmcnt(0) lgkmcnt(1)
	v_mfma_f32_32x32x16_f16 v[18:33], v[36:39], v[112:115], v[18:33]
	s_waitcnt lgkmcnt(0)
	v_mfma_f32_32x32x16_f16 v[2:17], v[40:43], v[112:115], v[2:17]
	s_nop 11
	v_max_f32_e32 v1, v19, v18
	v_max3_f32 v37, v20, v21, v3
	v_max3_f32 v1, v1, v2, v4
	v_max3_f32 v36, v37, v24, v25
	v_max3_f32 v1, v1, v5, v22
	v_max3_f32 v36, v36, v8, v9
	v_max3_f32 v1, v1, v23, v6
	v_max3_f32 v36, v36, v28, v29
	v_max3_f32 v1, v1, v7, v26
	v_max3_f32 v36, v36, v12, v13
	v_max3_f32 v1, v1, v27, v10
	v_max3_f32 v36, v36, v32, v33
	v_max3_f32 v1, v1, v11, v30
	v_max3_f32 v36, v36, v16, v17
	v_max3_f32 v1, v1, v31, v14
	v_max3_f32 v1, v1, v15, v36
	v_mov_b32_e32 v36, v1
	s_nop 1
	v_permlane32_swap_b32_e32 v1, v36
	v_max_f32_e32 v194, v36, v1
	v_lshlrev_b32_e32 v1, 1, v0
	v_sub_f32_e32 v36, v2, v194
	v_and_b32_e32 v1, 32, v1
	v_and_b32_e32 v2, 24, v190
	v_lshlrev_b32_e32 v0, 4, v0
	v_add3_u32 v1, 0, v1, v2
	v_and_b32_e32 v0, 0xc0, v0
	v_lshlrev_b32_e32 v2, 8, v46
	v_add3_u32 v192, v1, v2, v0
	v_xor_b32_e32 v0, 0x80000000, v194
	v_sub_f32_e32 v37, v3, v194
	v_sub_f32_e32 v38, v4, v194
	v_sub_f32_e32 v39, v5, v194
	v_sub_f32_e32 v40, v6, v194
	v_sub_f32_e32 v41, v7, v194
	v_sub_f32_e32 v42, v8, v194
	v_sub_f32_e32 v43, v9, v194
	v_sub_f32_e32 v47, v10, v194
	v_sub_f32_e32 v57, v11, v194
	v_sub_f32_e32 v58, v12, v194
	v_sub_f32_e32 v59, v13, v194
	v_sub_f32_e32 v60, v14, v194
	v_sub_f32_e32 v61, v15, v194
	v_mov_b32_e32 v1, v0
	v_mov_b32_e32 v2, v0
	v_mov_b32_e32 v3, v0
	v_mov_b32_e32 v4, v0
	v_mov_b32_e32 v5, v0
	v_mov_b32_e32 v6, v0
	v_mov_b32_e32 v7, v0
	v_mov_b32_e32 v8, v0
	v_mov_b32_e32 v9, v0
	v_mov_b32_e32 v10, v0
	v_mov_b32_e32 v11, v0
	v_mov_b32_e32 v12, v0
	v_mov_b32_e32 v13, v0
	v_mov_b32_e32 v14, v0
	v_mov_b32_e32 v15, v0
	s_waitcnt vmcnt(0) lgkmcnt(0)
	s_barrier
	v_sub_f32_e32 v62, v16, v194
	v_sub_f32_e32 v63, v17, v194
	v_lshl_add_u64 v[16:17], v[44:45], 0, s[12:13]
	s_mov_b32 s1, m0
	s_mov_b32 m0, s25
	s_nop 0
	global_load_lds_dwordx4 v[16:17], off
	s_mov_b32 m0, s1
	s_add_i32 s1, s25, 0xa000
	v_lshl_add_u64 v[16:17], v[34:35], 0, s[2:3]
	s_mov_b32 s11, m0
	s_mov_b32 m0, s1
	s_nop 0
	global_load_lds_dwordx4 v[16:17], off
	s_mov_b32 m0, s11
	ds_read_b128 v[172:175], v195 offset:8192
	ds_read_b128 v[168:171], v195 offset:8704
	ds_read_b128 v[164:167], v195 offset:10240
	ds_read_b128 v[160:163], v195 offset:10752
	ds_read_b128 v[156:159], v195 offset:12288
	ds_read_b128 v[152:155], v195 offset:12800
	ds_read_b128 v[148:151], v195 offset:14336
	ds_read_b128 v[144:147], v195 offset:14848
	s_add_i32 s11, s0, 0
	v_sub_f32_e32 v18, v18, v194
	v_sub_f32_e32 v19, v19, v194
	v_sub_f32_e32 v20, v20, v194
	v_sub_f32_e32 v21, v21, v194
	v_sub_f32_e32 v22, v22, v194
	v_sub_f32_e32 v23, v23, v194
	v_sub_f32_e32 v24, v24, v194
	v_sub_f32_e32 v25, v25, v194
	v_sub_f32_e32 v26, v26, v194
	v_sub_f32_e32 v27, v27, v194
	v_sub_f32_e32 v28, v28, v194
	v_sub_f32_e32 v29, v29, v194
	v_sub_f32_e32 v30, v30, v194
	v_sub_f32_e32 v31, v31, v194
	v_sub_f32_e32 v32, v32, v194
	v_sub_f32_e32 v33, v33, v194
	s_add_u32 s14, s16, s34
	v_exp_f32_e32 v64, v18
	v_exp_f32_e32 v65, v19
	v_exp_f32_e32 v48, v36
	v_exp_f32_e32 v49, v37
	v_exp_f32_e32 v66, v20
	v_exp_f32_e32 v50, v38
	v_exp_f32_e32 v67, v21
	v_exp_f32_e32 v51, v39
	v_exp_f32_e32 v68, v22
	v_exp_f32_e32 v52, v40
	v_exp_f32_e32 v69, v23
	v_exp_f32_e32 v53, v41
	v_exp_f32_e32 v70, v24
	v_exp_f32_e32 v54, v42
	v_exp_f32_e32 v71, v25
	v_exp_f32_e32 v55, v43
	v_exp_f32_e32 v72, v26
	v_exp_f32_e32 v56, v47
	v_exp_f32_e32 v73, v27
	v_exp_f32_e32 v57, v57
	v_exp_f32_e32 v74, v28
	v_exp_f32_e32 v58, v58
	v_exp_f32_e32 v75, v29
	v_exp_f32_e32 v59, v59
	v_exp_f32_e32 v76, v30
	v_exp_f32_e32 v60, v60
	v_exp_f32_e32 v77, v31
	v_exp_f32_e32 v61, v61
	v_exp_f32_e32 v78, v32
	v_exp_f32_e32 v62, v62
	v_exp_f32_e32 v79, v33
	v_exp_f32_e32 v63, v63
	s_addc_u32 s16, s17, s35
	s_waitcnt vmcnt(2) lgkmcnt(0)
	s_barrier
	v_or_b32_e32 v16, s14, v186
	v_mov_b32_e32 v17, s16
	v_lshl_add_u64 v[16:17], v[16:17], 0, s[18:19]
	v_cmp_gt_u32_e64 s[0:1], 32, v188
	v_lshl_add_u64 v[182:183], s[4:5], 0, v[16:17]
	v_lshl_add_u64 v[184:185], s[6:7], 0, v[16:17]
	s_mov_b32 s16, 0x41000000
	s_mov_b32 s36, 0x43800000
	s_mov_b64 s[4:5], 0x8000
	s_movk_i32 s14, 0x2000
	s_movk_i32 s19, 0x4000
	v_mov_b32_e32 v16, v187
	v_mov_b32_e32 v17, v187
	v_mov_b32_e32 v18, v187
	v_mov_b32_e32 v19, v187
	v_mov_b32_e32 v20, v187
	v_mov_b32_e32 v21, v187
	v_mov_b32_e32 v22, v187
	v_mov_b32_e32 v23, v187
	v_mov_b32_e32 v24, v187
	v_mov_b32_e32 v25, v187
	v_mov_b32_e32 v26, v187
	v_mov_b32_e32 v27, v187
	v_mov_b32_e32 v28, v187
	v_mov_b32_e32 v29, v187
	v_mov_b32_e32 v30, v187
	v_mov_b32_e32 v31, v187
	v_mov_b32_e32 v32, v187
	v_mov_b32_e32 v33, v187
	v_mov_b32_e32 v34, v187
	v_mov_b32_e32 v35, v187
	v_mov_b32_e32 v36, v187
	v_mov_b32_e32 v37, v187
	v_mov_b32_e32 v38, v187
	v_mov_b32_e32 v39, v187
	v_mov_b32_e32 v40, v187
	v_mov_b32_e32 v41, v187
	v_mov_b32_e32 v42, v187
	v_mov_b32_e32 v43, v187
	v_mov_b32_e32 v44, v187
	v_mov_b32_e32 v45, v187
	v_mov_b32_e32 v46, v187
	v_mov_b32_e32 v47, v187
	v_lshl_add_u32 v186, v189, 2, s11
.LBB2_1:
	s_mov_b32 s17, s31
	s_mov_b32 s18, s15
	v_add_u32_e32 v196, s18, v192
	ds_read_b64_tr_b16 v[176:177], v196 offset:24576
	ds_read_b64_tr_b16 v[178:179], v196 offset:25088
	s_waitcnt lgkmcnt(9)
	v_mfma_f32_32x32x16_f16 v[96:111], v[172:175], v[136:139], v[0:15]
	v_add_f32_e32 v80, v64, v65
	v_add_f32_e32 v80, v66, v80
	v_add_f32_e32 v80, v67, v80
	v_add_f32_e32 v80, v68, v80
	v_add_f32_e32 v80, v69, v80
	v_cvt_pk_f16_f32 v140, v64, v65
	v_cvt_pk_f16_f32 v141, v66, v67
	ds_read_b64_tr_b16 v[172:173], v196 offset:28672
	ds_read_b64_tr_b16 v[174:175], v196 offset:29184
	v_add_f32_e32 v64, v70, v80
	s_waitcnt lgkmcnt(10)
	v_mfma_f32_32x32x16_f16 v[80:95], v[168:171], v[136:139], v[0:15]
	v_add_f32_e32 v64, v71, v64
	v_add_f32_e32 v64, v72, v64
	v_add_f32_e32 v64, v73, v64
	v_cvt_pk_f16_f32 v142, v68, v69
	v_cvt_pk_f16_f32 v143, v70, v71
	ds_read_b64_tr_b16 v[68:69], v196 offset:25600
	ds_read_b64_tr_b16 v[70:71], v196 offset:26112
	s_waitcnt lgkmcnt(11)
	v_mfma_f32_32x32x16_f16 v[96:111], v[164:167], v[128:131], v[96:111]
	v_add_f32_e32 v64, v74, v64
	v_add_f32_e32 v64, v75, v64
	v_add_f32_e32 v64, v76, v64
	v_add_f32_e32 v116, v77, v64
	v_cvt_pk_f16_f32 v132, v72, v73
	v_cvt_pk_f16_f32 v133, v74, v75
	ds_read_b64_tr_b16 v[64:65], v196 offset:29696
	ds_read_b64_tr_b16 v[66:67], v196 offset:30208
	s_waitcnt lgkmcnt(12)
	v_mfma_f32_32x32x16_f16 v[80:95], v[160:163], v[128:131], v[80:95]
	v_add_f32_e32 v72, v78, v116
	v_add_f32_e32 v72, v79, v72
	v_add_f32_e32 v72, v48, v72
	v_add_f32_e32 v116, v49, v72
	v_cvt_pk_f16_f32 v134, v76, v77
	v_cvt_pk_f16_f32 v135, v78, v79
	ds_read_b64_tr_b16 v[72:73], v196 offset:26624
	ds_read_b64_tr_b16 v[74:75], v196 offset:27136
	s_waitcnt lgkmcnt(13)
	v_mfma_f32_32x32x16_f16 v[96:111], v[156:159], v[120:123], v[96:111]
	v_add_f32_e32 v76, v50, v116
	v_add_f32_e32 v76, v51, v76
	v_add_f32_e32 v76, v52, v76
	v_add_f32_e32 v76, v53, v76
	v_cvt_pk_f16_f32 v124, v48, v49
	v_cvt_pk_f16_f32 v125, v50, v51
	ds_read_b64_tr_b16 v[48:49], v196 offset:30720
	ds_read_b64_tr_b16 v[50:51], v196 offset:31232
	s_waitcnt lgkmcnt(14)
	v_mfma_f32_32x32x16_f16 v[80:95], v[152:155], v[120:123], v[80:95]
	v_add_f32_e32 v76, v54, v76
	v_add_f32_e32 v76, v55, v76
	v_add_f32_e32 v76, v56, v76
	v_add_f32_e32 v76, v57, v76
	v_cvt_pk_f16_f32 v126, v52, v53
	v_cvt_pk_f16_f32 v127, v54, v55
	ds_read_b64_tr_b16 v[52:53], v196 offset:27648
	ds_read_b64_tr_b16 v[54:55], v196 offset:28160
	s_waitcnt lgkmcnt(14)
	v_mfma_f32_32x32x16_f16 v[96:111], v[148:151], v[112:115], v[96:111]
	v_add_f32_e32 v76, v58, v76
	v_add_f32_e32 v76, v59, v76
	v_add_f32_e32 v76, v60, v76
	v_add_f32_e32 v76, v61, v76
	v_cvt_pk_f16_f32 v116, v56, v57
	v_cvt_pk_f16_f32 v117, v58, v59
	ds_read_b64_tr_b16 v[56:57], v196 offset:31744
	ds_read_b64_tr_b16 v[58:59], v196 offset:32256
	v_mfma_f32_32x32x16_f16 v[80:95], v[144:147], v[112:115], v[80:95]
	v_add_f32_e32 v76, v62, v76
	v_add_f32_e32 v76, v63, v76
	v_cvt_pk_f16_f32 v118, v60, v61
	v_cvt_pk_f16_f32 v119, v62, v63
	v_lshl_add_u64 v[60:61], v[182:183], 0, s[12:13]
	s_add_i32 s6, s14, s25
	s_mov_b32 s7, m0
	s_mov_b32 m0, s6
	s_nop 0
	global_load_lds_dwordx4 v[60:61], off
	s_mov_b32 m0, s7
	v_cmp_lt_f32_e32 vcc, s36, v76
	s_add_i32 s6, s28, s26
	s_mov_b32 s7, m0
	s_mov_b32 m0, s6
	s_nop 0
	global_load_lds_dwordx4 v[180:181], off
	s_mov_b32 m0, s7
	s_cbranch_vccnz .Lmy_rare_1
.Lmy_back_1:
	v_add_f32_e32 v187, v187, v76

.LBB2_4:
	v_add_u32_e32 v196, s17, v192
	ds_read_b64_tr_b16 v[144:145], v196 offset:24576
	ds_read_b64_tr_b16 v[146:147], v196 offset:25088
	s_waitcnt lgkmcnt(9)
	v_mfma_f32_32x32x16_f16 v[64:79], v[60:63], v[136:139], v[0:15]
	v_add_f32_e32 v48, v96, v97
	v_add_f32_e32 v48, v98, v48
	v_add_f32_e32 v48, v99, v48
	v_add_f32_e32 v48, v100, v48
	v_add_f32_e32 v48, v101, v48
	v_cvt_pk_f16_f32 v140, v96, v97
	v_cvt_pk_f16_f32 v141, v98, v99
	ds_read_b64_tr_b16 v[152:153], v196 offset:28672
	ds_read_b64_tr_b16 v[154:155], v196 offset:29184
	v_add_f32_e32 v48, v102, v48
	v_add_f32_e32 v48, v103, v48
	v_add_f32_e32 v48, v104, v48
	v_add_f32_e32 v96, v105, v48
	s_waitcnt lgkmcnt(10)
	v_mfma_f32_32x32x16_f16 v[48:63], v[148:151], v[136:139], v[0:15]
	v_cvt_pk_f16_f32 v142, v100, v101
	v_cvt_pk_f16_f32 v143, v102, v103
	ds_read_b64_tr_b16 v[148:149], v196 offset:25600
	ds_read_b64_tr_b16 v[150:151], v196 offset:26112
	s_waitcnt lgkmcnt(11)
	v_mfma_f32_32x32x16_f16 v[64:79], v[176:179], v[128:131], v[64:79]
	v_add_f32_e32 v96, v106, v96
	v_add_f32_e32 v96, v107, v96
	v_add_f32_e32 v96, v108, v96
	v_add_f32_e32 v96, v109, v96
	v_cvt_pk_f16_f32 v132, v104, v105
	v_cvt_pk_f16_f32 v133, v106, v107
	ds_read_b64_tr_b16 v[100:101], v196 offset:29696
	ds_read_b64_tr_b16 v[102:103], v196 offset:30208
	s_waitcnt lgkmcnt(12)
	v_mfma_f32_32x32x16_f16 v[48:63], v[172:175], v[128:131], v[48:63]
	v_add_f32_e32 v96, v110, v96
	v_add_f32_e32 v96, v111, v96
	v_add_f32_e32 v96, v80, v96
	v_add_f32_e32 v104, v81, v96
	v_cvt_pk_f16_f32 v134, v108, v109
	v_cvt_pk_f16_f32 v135, v110, v111
	ds_read_b64_tr_b16 v[96:97], v196 offset:26624
	ds_read_b64_tr_b16 v[98:99], v196 offset:27136
	s_waitcnt lgkmcnt(13)
	v_mfma_f32_32x32x16_f16 v[64:79], v[168:171], v[120:123], v[64:79]
	v_add_f32_e32 v104, v82, v104
	v_add_f32_e32 v104, v83, v104
	v_add_f32_e32 v104, v84, v104
	v_add_f32_e32 v104, v85, v104
	v_cvt_pk_f16_f32 v124, v80, v81
	v_cvt_pk_f16_f32 v125, v82, v83
	ds_read_b64_tr_b16 v[80:81], v196 offset:30720
	ds_read_b64_tr_b16 v[82:83], v196 offset:31232
	s_waitcnt lgkmcnt(14)
	v_mfma_f32_32x32x16_f16 v[48:63], v[164:167], v[120:123], v[48:63]
	v_add_f32_e32 v104, v86, v104
	v_add_f32_e32 v104, v87, v104
	v_add_f32_e32 v104, v88, v104
	v_add_f32_e32 v104, v89, v104
	v_cvt_pk_f16_f32 v126, v84, v85
	v_cvt_pk_f16_f32 v127, v86, v87
	ds_read_b64_tr_b16 v[84:85], v196 offset:27648
	ds_read_b64_tr_b16 v[86:87], v196 offset:28160
	s_waitcnt lgkmcnt(14)
	v_mfma_f32_32x32x16_f16 v[64:79], v[160:163], v[112:115], v[64:79]
	v_add_f32_e32 v104, v90, v104
	v_add_f32_e32 v104, v91, v104
	v_add_f32_e32 v104, v92, v104
	v_add_f32_e32 v104, v93, v104
	v_cvt_pk_f16_f32 v116, v88, v89
	v_cvt_pk_f16_f32 v117, v90, v91
	ds_read_b64_tr_b16 v[88:89], v196 offset:31744
	ds_read_b64_tr_b16 v[90:91], v196 offset:32256
	v_mfma_f32_32x32x16_f16 v[48:63], v[156:159], v[112:115], v[48:63]
	v_add_f32_e32 v104, v94, v104
	v_add_f32_e32 v104, v95, v104
	v_cvt_pk_f16_f32 v118, v92, v93
	v_cvt_pk_f16_f32 v119, v94, v95
	v_lshl_add_u64 v[92:93], v[182:183], 0, s[4:5]
	s_add_i32 s6, s19, s25
	s_mov_b32 s7, m0
	s_mov_b32 m0, s6
	s_nop 0
	global_load_lds_dwordx4 v[92:93], off
	s_mov_b32 m0, s7
	v_cmp_lt_f32_e32 vcc, s36, v104
	v_lshl_add_u64 v[92:93], v[184:185], 0, s[12:13]
	s_add_i32 s6, s18, s26
	s_mov_b32 s7, m0
	s_mov_b32 m0, s6
	s_nop 0
	global_load_lds_dwordx4 v[92:93], off
	s_mov_b32 m0, s7
	s_cbranch_vccnz .Lmy_rare_2
.Lmy_back_2:
	v_add_f32_e32 v187, v187, v104
.LBB2_5:
	s_add_i32 s14, s19, 0x2000
	s_cmpk_lg_i32 s19, 0x4000
	s_cselect_b32 s14, s14, 0
	s_waitcnt lgkmcnt(14)
	v_mfma_f32_32x32x16_f16 v[16:31], v[140:143], v[144:147], v[16:31]
	v_exp_f32_e32 v64, v64
	v_exp_f32_e32 v65, v65
	v_exp_f32_e32 v66, v66
	v_exp_f32_e32 v67, v67
	s_waitcnt lgkmcnt(12)
	v_mfma_f32_32x32x16_f16 v[32:47], v[140:143], v[152:155], v[32:47]
	v_exp_f32_e32 v68, v68
	v_exp_f32_e32 v69, v69
	v_exp_f32_e32 v70, v70
	v_exp_f32_e32 v71, v71
	v_add_u32_e32 v92, s14, v195
	ds_read_b128 v[172:175], v92
	ds_read_b128 v[168:171], v92 offset:512
	s_waitcnt lgkmcnt(12)
	v_mfma_f32_32x32x16_f16 v[16:31], v[132:135], v[148:151], v[16:31]
	v_exp_f32_e32 v72, v72
	v_exp_f32_e32 v73, v73
	v_exp_f32_e32 v74, v74
	v_exp_f32_e32 v75, v75
	ds_read_b128 v[164:167], v92 offset:2048
	ds_read_b128 v[160:163], v92 offset:2560
	s_waitcnt lgkmcnt(12)
	v_mfma_f32_32x32x16_f16 v[32:47], v[132:135], v[100:103], v[32:47]
	v_exp_f32_e32 v76, v76
	v_exp_f32_e32 v77, v77
	v_exp_f32_e32 v78, v78
	v_exp_f32_e32 v79, v79
	ds_read_b128 v[156:159], v92 offset:4096
	ds_read_b128 v[152:155], v92 offset:4608
	s_waitcnt lgkmcnt(12)
	v_mfma_f32_32x32x16_f16 v[16:31], v[124:127], v[96:99], v[16:31]
	v_exp_f32_e32 v48, v48
	v_exp_f32_e32 v49, v49
	v_exp_f32_e32 v50, v50
	v_exp_f32_e32 v51, v51
	ds_read_b128 v[148:151], v92 offset:6144
	ds_read_b128 v[144:147], v92 offset:6656
	s_waitcnt lgkmcnt(12)
	v_mfma_f32_32x32x16_f16 v[32:47], v[124:127], v[80:83], v[32:47]
	v_exp_f32_e32 v52, v52
	v_exp_f32_e32 v53, v53
	v_exp_f32_e32 v54, v54
	v_exp_f32_e32 v55, v55
	s_waitcnt lgkmcnt(10)
	v_mfma_f32_32x32x16_f16 v[16:31], v[116:119], v[84:87], v[16:31]
	v_exp_f32_e32 v56, v56
	v_exp_f32_e32 v57, v57
	v_exp_f32_e32 v58, v58
	v_exp_f32_e32 v59, v59
	s_waitcnt lgkmcnt(8)
	v_mfma_f32_32x32x16_f16 v[32:47], v[116:119], v[88:91], v[32:47]
	v_exp_f32_e32 v60, v60
	v_exp_f32_e32 v61, v61
	v_exp_f32_e32 v62, v62
	v_exp_f32_e32 v63, v63
	s_waitcnt vmcnt(3) lgkmcnt(0)
	s_barrier
.LBB2_7:
	s_add_i32 s6, s14, 0x2000
	s_cmpk_lg_i32 s14, 0x4000
	s_cselect_b32 s19, s6, 0
	s_add_i32 s27, s27, 2
	v_lshl_add_u64 v[180:181], v[180:181], 0, s[2:3]
	v_lshl_add_u64 v[182:183], v[182:183], 0, s[2:3]
	s_cmp_gt_u32 s27, 28
	v_lshl_add_u64 v[184:185], v[184:185], 0, s[2:3]
	s_cbranch_scc1 .LBB2_15
	s_mov_b32 s15, s29
	s_mov_b32 s31, s28
	s_mov_b32 s29, s18
	s_mov_b32 s28, s17
	s_branch .LBB2_1
.LBB2_15:
	ds_read_b64_tr_b16 v[96:97], v192 offset:40960
	ds_read_b64_tr_b16 v[98:99], v192 offset:41472
	v_add_f32_e32 v80, v64, v65
	v_add_f32_e32 v80, v66, v80
	v_add_f32_e32 v80, v67, v80
	v_add_f32_e32 v80, v68, v80
	v_add_f32_e32 v100, v69, v80
	s_waitcnt lgkmcnt(9)
	v_mfma_f32_32x32x16_f16 v[80:95], v[172:175], v[136:139], v[0:15]
	v_cvt_pk_f16_f32 v140, v64, v65
	v_cvt_pk_f16_f32 v141, v66, v67
	ds_read_b64_tr_b16 v[64:65], v192 offset:45056
	ds_read_b64_tr_b16 v[66:67], v192 offset:45568
	s_waitcnt lgkmcnt(10)
	v_mfma_f32_32x32x16_f16 v[0:15], v[168:171], v[136:139], v[0:15]
	v_add_f32_e32 v100, v70, v100
	v_add_f32_e32 v100, v71, v100
	v_add_f32_e32 v100, v72, v100
	v_add_f32_e32 v100, v73, v100
	v_cvt_pk_f16_f32 v142, v68, v69
	v_cvt_pk_f16_f32 v143, v70, v71
	ds_read_b64_tr_b16 v[68:69], v192 offset:41984
	ds_read_b64_tr_b16 v[70:71], v192 offset:42496
	s_waitcnt lgkmcnt(11)
	v_mfma_f32_32x32x16_f16 v[80:95], v[164:167], v[128:131], v[80:95]
	v_add_f32_e32 v100, v74, v100
	v_add_f32_e32 v100, v75, v100
	v_add_f32_e32 v100, v76, v100
	v_add_f32_e32 v100, v77, v100
	v_cvt_pk_f16_f32 v132, v72, v73
	v_cvt_pk_f16_f32 v133, v74, v75
	ds_read_b64_tr_b16 v[72:73], v192 offset:46080
	ds_read_b64_tr_b16 v[74:75], v192 offset:46592
	s_waitcnt lgkmcnt(12)
	v_mfma_f32_32x32x16_f16 v[0:15], v[160:163], v[128:131], v[0:15]
	v_add_f32_e32 v100, v78, v100
	v_add_f32_e32 v100, v79, v100
	v_add_f32_e32 v100, v48, v100
	v_add_f32_e32 v100, v49, v100
	v_cvt_pk_f16_f32 v134, v76, v77
	v_cvt_pk_f16_f32 v135, v78, v79
	ds_read_b64_tr_b16 v[76:77], v192 offset:43008
	ds_read_b64_tr_b16 v[78:79], v192 offset:43520
	s_waitcnt lgkmcnt(13)
	v_mfma_f32_32x32x16_f16 v[80:95], v[156:159], v[120:123], v[80:95]
	v_add_f32_e32 v100, v50, v100
	v_add_f32_e32 v100, v51, v100
	v_add_f32_e32 v100, v52, v100
	v_add_f32_e32 v104, v53, v100
	v_cvt_pk_f16_f32 v124, v48, v49
	v_cvt_pk_f16_f32 v125, v50, v51
	ds_read_b64_tr_b16 v[100:101], v192 offset:47104
	ds_read_b64_tr_b16 v[102:103], v192 offset:47616
	s_waitcnt lgkmcnt(14)
	v_mfma_f32_32x32x16_f16 v[0:15], v[152:155], v[120:123], v[0:15]
	v_add_f32_e32 v48, v54, v104
	v_add_f32_e32 v48, v55, v48
	v_add_f32_e32 v48, v56, v48
	v_add_f32_e32 v48, v57, v48
	v_cvt_pk_f16_f32 v126, v52, v53
	v_cvt_pk_f16_f32 v127, v54, v55
	ds_read_b64_tr_b16 v[104:105], v192 offset:44032
	ds_read_b64_tr_b16 v[106:107], v192 offset:44544
	s_waitcnt lgkmcnt(14)
	v_mfma_f32_32x32x16_f16 v[80:95], v[148:151], v[112:115], v[80:95]
	v_add_f32_e32 v48, v58, v48
	v_add_f32_e32 v48, v59, v48
	v_add_f32_e32 v48, v60, v48
	v_add_f32_e32 v48, v61, v48
	v_cvt_pk_f16_f32 v116, v56, v57
	v_cvt_pk_f16_f32 v117, v58, v59
	ds_read_b64_tr_b16 v[108:109], v192 offset:48128
	ds_read_b64_tr_b16 v[110:111], v192 offset:48640
	v_mfma_f32_32x32x16_f16 v[0:15], v[144:147], v[112:115], v[0:15]
	v_add_f32_e32 v48, v62, v48
	v_add_f32_e32 v48, v63, v48
	v_cvt_pk_f16_f32 v118, v60, v61
	v_cvt_pk_f16_f32 v119, v62, v63
	s_nop 0
	v_cmp_lt_f32_e32 vcc, s36, v48
	s_nop 4
	s_cbranch_vccnz .Lmy_rare_3
.Lmy_back_3:
	v_add_f32_e32 v253, v187, v48
	s_nop 7
	s_nop 3
.LBB2_16:
	s_waitcnt lgkmcnt(14)
	v_mfma_f32_32x32x16_f16 v[16:31], v[140:143], v[96:99], v[16:31]
	v_exp_f32_e32 v80, v80
	v_exp_f32_e32 v81, v81
	v_exp_f32_e32 v82, v82
	v_exp_f32_e32 v83, v83
	s_waitcnt lgkmcnt(12)
	v_mfma_f32_32x32x16_f16 v[32:47], v[140:143], v[64:67], v[32:47]
	v_exp_f32_e32 v84, v84
	v_exp_f32_e32 v85, v85
	v_exp_f32_e32 v86, v86
	v_exp_f32_e32 v87, v87
	s_waitcnt lgkmcnt(10)
	v_mfma_f32_32x32x16_f16 v[16:31], v[132:135], v[68:71], v[16:31]
	v_exp_f32_e32 v88, v88
	v_exp_f32_e32 v89, v89
	v_exp_f32_e32 v90, v90
	v_exp_f32_e32 v91, v91
	s_waitcnt lgkmcnt(8)
	v_mfma_f32_32x32x16_f16 v[32:47], v[132:135], v[72:75], v[32:47]
	v_exp_f32_e32 v92, v92
	v_exp_f32_e32 v93, v93
	v_exp_f32_e32 v94, v94
	v_exp_f32_e32 v95, v95
	s_waitcnt lgkmcnt(6)
	v_mfma_f32_32x32x16_f16 v[16:31], v[124:127], v[76:79], v[16:31]
	v_exp_f32_e32 v0, v0
	v_exp_f32_e32 v1, v1
	v_exp_f32_e32 v2, v2
	v_exp_f32_e32 v3, v3
	s_waitcnt lgkmcnt(4)
	v_mfma_f32_32x32x16_f16 v[32:47], v[124:127], v[100:103], v[32:47]
	v_exp_f32_e32 v4, v4
	v_exp_f32_e32 v5, v5
	v_exp_f32_e32 v6, v6
	v_exp_f32_e32 v7, v7
	s_waitcnt lgkmcnt(2)
	v_mfma_f32_32x32x16_f16 v[16:31], v[116:119], v[104:107], v[16:31]
	v_exp_f32_e32 v8, v8
	v_exp_f32_e32 v9, v9
	v_exp_f32_e32 v10, v10
	v_exp_f32_e32 v11, v11
	s_waitcnt lgkmcnt(0)
	v_mfma_f32_32x32x16_f16 v[32:47], v[116:119], v[108:111], v[32:47]
	v_exp_f32_e32 v12, v12
	v_exp_f32_e32 v13, v13
	v_exp_f32_e32 v14, v14
	v_exp_f32_e32 v15, v15
	v_add_u32_e32 v48, s11, v193
.LBB2_18:
	s_waitcnt vmcnt(0) lgkmcnt(0)
	s_barrier
	v_add_f32_e32 v248, v80, v81
	v_add_f32_e32 v248, v82, v248
	v_add_f32_e32 v248, v83, v248
	v_add_f32_e32 v248, v84, v248
	v_add_f32_e32 v248, v85, v248
	v_add_f32_e32 v248, v86, v248
	v_add_f32_e32 v248, v87, v248
	v_add_f32_e32 v248, v88, v248
	v_add_f32_e32 v248, v89, v248
	v_add_f32_e32 v248, v90, v248
	v_add_f32_e32 v248, v91, v248
	v_add_f32_e32 v248, v92, v248
	v_add_f32_e32 v248, v93, v248
	v_add_f32_e32 v248, v94, v248
	v_add_f32_e32 v248, v95, v248
	v_add_f32_e32 v248, v0, v248
	v_add_f32_e32 v248, v1, v248
	v_add_f32_e32 v248, v2, v248
	v_add_f32_e32 v248, v3, v248
	v_add_f32_e32 v248, v4, v248
	v_add_f32_e32 v248, v5, v248
	v_add_f32_e32 v248, v6, v248
	v_add_f32_e32 v248, v7, v248
	v_add_f32_e32 v248, v8, v248
	v_add_f32_e32 v248, v9, v248
	v_add_f32_e32 v248, v10, v248
	v_add_f32_e32 v248, v11, v248
	v_add_f32_e32 v248, v12, v248
	v_add_f32_e32 v248, v13, v248
	v_add_f32_e32 v248, v14, v248
	v_add_f32_e32 v248, v15, v248
	v_cmp_lt_f32_e32 vcc, s36, v248
	s_nop 4
	s_cbranch_vccnz .Lmy_rare_4
.Lmy_back_4:
	ds_read_b64_tr_b16 v[54:55], v192 offset:49152
	ds_read_b64_tr_b16 v[56:57], v192 offset:49664
	v_add_f32_e32 v49, v80, v81
	v_cvt_pk_f16_f32 v50, v80, v81
	v_cvt_pk_f16_f32 v51, v82, v83
	v_cvt_pk_f16_f32 v52, v84, v85
	v_cvt_pk_f16_f32 v53, v86, v87
	ds_read_b64_tr_b16 v[58:59], v192 offset:50176
	ds_read_b64_tr_b16 v[60:61], v192 offset:50688
	s_waitcnt lgkmcnt(2)
	v_mfma_f32_32x32x16_f16 v[16:31], v[50:53], v[54:57], v[16:31]
	ds_read_b64_tr_b16 v[54:55], v192 offset:53248
	ds_read_b64_tr_b16 v[56:57], v192 offset:53760
	v_add_f32_e32 v49, v82, v49
	v_add_f32_e32 v49, v83, v49
	v_add_f32_e32 v49, v84, v49
	v_add_f32_e32 v49, v85, v49
	v_add_f32_e32 v49, v86, v49
	v_add_f32_e32 v49, v87, v49
	s_waitcnt lgkmcnt(0)
	v_mfma_f32_32x32x16_f16 v[32:47], v[50:53], v[54:57], v[32:47]
	v_add_f32_e32 v49, v88, v49
	v_add_f32_e32 v49, v89, v49
	ds_read_b64_tr_b16 v[62:63], v192 offset:54272
	ds_read_b64_tr_b16 v[64:65], v192 offset:54784
	v_add_f32_e32 v49, v90, v49
	v_add_f32_e32 v49, v91, v49
	v_cvt_pk_f16_f32 v50, v88, v89
	v_cvt_pk_f16_f32 v51, v90, v91
	v_cvt_pk_f16_f32 v52, v92, v93
	v_cvt_pk_f16_f32 v53, v94, v95
	v_add_f32_e32 v49, v92, v49
	v_mfma_f32_32x32x16_f16 v[16:31], v[50:53], v[58:61], v[16:31]
	v_add_f32_e32 v49, v93, v49
	v_add_f32_e32 v49, v94, v49
	v_add_f32_e32 v49, v95, v49
	v_add_f32_e32 v49, v0, v49
	v_add_f32_e32 v49, v1, v49
	v_add_f32_e32 v49, v2, v49
	v_add_f32_e32 v49, v3, v49
	s_waitcnt lgkmcnt(0)
	v_mfma_f32_32x32x16_f16 v[32:47], v[50:53], v[62:65], v[32:47]
	ds_read_b64_tr_b16 v[50:51], v192 offset:51200
	ds_read_b64_tr_b16 v[52:53], v192 offset:51712
	v_cvt_pk_f16_f32 v0, v0, v1
	v_cvt_pk_f16_f32 v1, v2, v3
	v_cvt_pk_f16_f32 v2, v4, v5
	v_cvt_pk_f16_f32 v3, v6, v7
	ds_read_b64_tr_b16 v[54:55], v192 offset:52224
	ds_read_b64_tr_b16 v[56:57], v192 offset:52736
	v_add_f32_e32 v4, v4, v49
	s_waitcnt lgkmcnt(2)
	v_mfma_f32_32x32x16_f16 v[16:31], v[0:3], v[50:53], v[16:31]
	ds_read_b64_tr_b16 v[50:51], v192 offset:55296
	ds_read_b64_tr_b16 v[52:53], v192 offset:55808
	v_add_f32_e32 v4, v5, v4
	v_add_f32_e32 v4, v6, v4
	ds_read_b64_tr_b16 v[58:59], v192 offset:56320
	ds_read_b64_tr_b16 v[60:61], v192 offset:56832
	v_cvt_pk_f16_f32 v5, v14, v15
	s_waitcnt lgkmcnt(2)
	v_mfma_f32_32x32x16_f16 v[32:47], v[0:3], v[50:53], v[32:47]
	v_add_f32_e32 v0, v7, v4
	v_add_f32_e32 v0, v8, v0
	v_add_f32_e32 v0, v9, v0
	v_add_f32_e32 v0, v10, v0
	v_cvt_pk_f16_f32 v2, v8, v9
	v_cvt_pk_f16_f32 v3, v10, v11
	v_cvt_pk_f16_f32 v4, v12, v13
	v_add_f32_e32 v0, v11, v0
	v_mfma_f32_32x32x16_f16 v[16:31], v[2:5], v[54:57], v[16:31]
	v_add_f32_e32 v0, v12, v0
	v_add_f32_e32 v0, v13, v0
	v_add_f32_e32 v0, v14, v0
	v_add_f32_e32 v0, v15, v0
	v_add_f32_e32 v0, v253, v0
	v_mov_b32_e32 v1, v0
	s_nop 1
	v_permlane32_swap_b32_e32 v0, v1
	s_waitcnt lgkmcnt(0)
	v_mfma_f32_32x32x16_f16 v[32:47], v[2:5], v[58:61], v[32:47]
	s_and_saveexec_b64 s[2:3], s[0:1]
	v_add_f32_e32 v0, v0, v1
	ds_write_b32 v186, v0 offset:57472
	s_or_b64 exec, exec, s[2:3]
	s_waitcnt lgkmcnt(0)
	ds_read_b128 v[0:3], v48 offset:57472
	ds_read_b128 v[4:7], v48 offset:57504
	s_mov_b32 s11, 0
	s_lshl_b64 s[0:1], s[10:11], 22
	s_add_u32 s0, s8, s0
	s_waitcnt lgkmcnt(1)
	v_rcp_f32_e32 v8, v0
	v_rcp_f32_e32 v9, v1
	s_addc_u32 s1, s9, s1
	s_lshl_b32 s2, s23, 12
	v_rcp_f32_e32 v10, v2
	v_rcp_f32_e32 v11, v3
	s_waitcnt lgkmcnt(0)
	v_rcp_f32_e32 v12, v4
	ds_read_b128 v[0:3], v48 offset:57536
	v_rcp_f32_e32 v13, v5
	v_rcp_f32_e32 v14, v6
	v_rcp_f32_e32 v15, v7
	ds_read_b128 v[4:7], v48 offset:57568
	s_add_i32 s6, s2, 0
	v_lshlrev_b32_e32 v48, 1, v189
	v_add3_u32 v48, s6, v191, v48
	v_fma_mixlo_f16 v16, v16, v8, 0
	v_fma_mixlo_f16 v8, v32, v8, 0
	ds_write_b16 v48, v8 offset:59456
	v_fma_mixlo_f16 v8, v17, v9, 0
	ds_write_b16 v48, v8 offset:59520
	v_fma_mixlo_f16 v8, v33, v9, 0
	ds_write_b16 v48, v8 offset:59584
	v_fma_mixlo_f16 v8, v18, v10, 0
	ds_write_b16 v48, v8 offset:59648
	v_fma_mixlo_f16 v8, v34, v10, 0
	ds_write_b16 v48, v8 offset:59712
	v_fma_mixlo_f16 v8, v19, v11, 0
	ds_write_b16 v48, v8 offset:59776
	v_fma_mixlo_f16 v8, v35, v11, 0
	ds_write_b16 v48, v8 offset:59840
	v_fma_mixlo_f16 v8, v20, v12, 0
	ds_write_b16 v48, v8 offset:60416
	v_fma_mixlo_f16 v8, v36, v12, 0
	ds_write_b16 v48, v8 offset:60480
	v_fma_mixlo_f16 v8, v21, v13, 0
	ds_write_b16 v48, v8 offset:60544
	v_fma_mixlo_f16 v8, v37, v13, 0
	s_waitcnt lgkmcnt(11)
	v_rcp_f32_e32 v0, v0
	ds_write_b16 v48, v8 offset:60608
	v_fma_mixlo_f16 v8, v22, v14, 0
	v_rcp_f32_e32 v1, v1
	ds_write_b16 v48, v8 offset:60672
	v_fma_mixlo_f16 v8, v38, v14, 0
	ds_write_b16 v48, v8 offset:60736
	v_fma_mixlo_f16 v8, v23, v15, 0
	v_rcp_f32_e32 v2, v2
	ds_write_b16 v48, v8 offset:60800
	v_fma_mixlo_f16 v8, v39, v15, 0
	ds_write_b16 v48, v8 offset:60864
	v_fma_mixlo_f16 v8, v24, v0, 0
	v_fma_mixlo_f16 v0, v40, v0, 0
	v_rcp_f32_e32 v3, v3
	ds_write_b16 v48, v0 offset:61504
	v_fma_mixlo_f16 v0, v25, v1, 0
	ds_write_b16 v48, v0 offset:61568
	v_fma_mixlo_f16 v0, v41, v1, 0
	s_waitcnt lgkmcnt(14)
	v_rcp_f32_e32 v4, v4
	ds_write_b16 v48, v0 offset:61632
	v_fma_mixlo_f16 v0, v26, v2, 0
	ds_write_b16 v48, v0 offset:61696
	v_fma_mixlo_f16 v0, v42, v2, 0
	v_rcp_f32_e32 v5, v5
	ds_write_b16 v48, v0 offset:61760
	v_fma_mixlo_f16 v0, v27, v3, 0
	ds_write_b16 v48, v0 offset:61824
	v_fma_mixlo_f16 v0, v43, v3, 0
	v_rcp_f32_e32 v6, v6
	ds_write_b16 v48, v0 offset:61888
	v_fma_mixlo_f16 v0, v28, v4, 0
	ds_write_b16 v48, v0 offset:62464
	v_fma_mixlo_f16 v0, v44, v4, 0
	v_rcp_f32_e32 v7, v7
	ds_write_b16 v48, v0 offset:62528
	v_fma_mixlo_f16 v0, v29, v5, 0
	ds_write_b16 v48, v0 offset:62592
	v_fma_mixlo_f16 v0, v45, v5, 0
	ds_write_b16 v48, v0 offset:62656
	v_fma_mixlo_f16 v0, v30, v6, 0
	ds_write_b16 v48, v0 offset:62720
	v_fma_mixlo_f16 v0, v46, v6, 0
	ds_write_b16 v48, v0 offset:62784
	v_fma_mixlo_f16 v0, v31, v7, 0
	ds_write_b16 v48, v0 offset:62848
	v_fma_mixlo_f16 v0, v47, v7, 0
	ds_write_b16 v48, v0 offset:62912
	v_lshrrev_b32_e32 v0, 3, v188
	v_and_b32_e32 v4, 56, v190
	s_lshl_b32 s4, s24, 8
	s_lshl_b32 s5, s22, 9
	ds_write_b16 v48, v16 offset:59392
	ds_write_b16 v48, v8 offset:61440
	v_lshlrev_b32_e32 v1, 7, v0
	v_lshlrev_b32_e32 v2, 1, v4
	s_waitcnt lgkmcnt(0)
	v_add3_u32 v8, s6, v1, v2
	s_or_b32 s4, s4, s5
	v_or_b32_e32 v5, s4, v0
	ds_read_b128 v[0:3], v8 offset:59392
	s_lshl_b32 s7, s20, 6
	v_add_lshl_u32 v5, v5, s21, 8
	v_or3_b32 v4, v5, s7, v4
	s_and_b32 s1, s1, 0xffff
	s_mov_b32 s3, 0x20000
	s_mov_b32 s2, 0x400000
	v_lshlrev_b32_e32 v12, 1, v4
	ds_read_b128 v[4:7], v8 offset:60416
	s_waitcnt lgkmcnt(1)
	buffer_store_dwordx4 v[0:3], v12, s[0:3], 0 offen sc1
	ds_read_b128 v[0:3], v8 offset:61440
	ds_read_b128 v[8:11], v8 offset:62464
	v_add_u32_e32 v13, 0x1000, v12
	s_waitcnt lgkmcnt(2)
	buffer_store_dwordx4 v[4:7], v13, s[0:3], 0 offen sc1
	s_nop 1
	v_add_u32_e32 v4, 0x2000, v12
	s_waitcnt lgkmcnt(1)
	buffer_store_dwordx4 v[0:3], v4, s[0:3], 0 offen sc1
	s_nop 1
	v_add_u32_e32 v0, 0x3000, v12
	s_waitcnt lgkmcnt(0)
	buffer_store_dwordx4 v[8:11], v0, s[0:3], 0 offen sc1
	s_waitcnt lgkmcnt(0)
	s_barrier
	s_endpgm
.Lmy_rare_1:
	v_subrev_u32_e32 v248, s25, v191
	v_add_u32_e32 v248, 0xffffe000, v248
	v_ashrrev_i32_e32 v249, 31, v248
	v_lshl_add_u64 v[250:251], v[182:183], 0, v[248:249]
	s_mov_b64 s[38:39], 0x1000
	v_lshl_add_u64 v[254:255], v[250:251], 0, s[38:39]
	v_xor_b32_e32 v252, 0x80000000, v194
	global_load_dwordx4 v[200:203], v[250:251], off
	global_load_dwordx4 v[204:207], v[250:251], off offset:2048
	global_load_dwordx4 v[208:211], v[254:255], off
	global_load_dwordx4 v[212:215], v[254:255], off offset:2048
	v_mov_b32_e32 v216, v252
	v_mov_b32_e32 v217, v252
	v_mov_b32_e32 v218, v252
	v_mov_b32_e32 v219, v252
	v_mov_b32_e32 v220, v252
	v_mov_b32_e32 v221, v252
	v_mov_b32_e32 v222, v252
	v_mov_b32_e32 v223, v252
	v_mov_b32_e32 v224, v252
	v_mov_b32_e32 v225, v252
	v_mov_b32_e32 v226, v252
	v_mov_b32_e32 v227, v252
	v_mov_b32_e32 v228, v252
	v_mov_b32_e32 v229, v252
	v_mov_b32_e32 v230, v252
	v_mov_b32_e32 v231, v252
	v_mov_b32_e32 v232, v252
	v_mov_b32_e32 v233, v252
	v_mov_b32_e32 v234, v252
	v_mov_b32_e32 v235, v252
	v_mov_b32_e32 v236, v252
	v_mov_b32_e32 v237, v252
	v_mov_b32_e32 v238, v252
	v_mov_b32_e32 v239, v252
	v_mov_b32_e32 v240, v252
	v_mov_b32_e32 v241, v252
	v_mov_b32_e32 v242, v252
	v_mov_b32_e32 v243, v252
	v_mov_b32_e32 v244, v252
	v_mov_b32_e32 v245, v252
	v_mov_b32_e32 v246, v252
	v_mov_b32_e32 v247, v252
	s_waitcnt vmcnt(0)
	v_mfma_f32_32x32x16_f16 v[216:231], v[200:203], v[136:139], v[216:231]
	v_mfma_f32_32x32x16_f16 v[216:231], v[204:207], v[128:131], v[216:231]
	v_mfma_f32_32x32x16_f16 v[216:231], v[208:211], v[120:123], v[216:231]
	v_mfma_f32_32x32x16_f16 v[216:231], v[212:215], v[112:115], v[216:231]
	global_load_dwordx4 v[200:203], v[250:251], off offset:512
	global_load_dwordx4 v[204:207], v[250:251], off offset:2560
	global_load_dwordx4 v[208:211], v[254:255], off offset:512
	global_load_dwordx4 v[212:215], v[254:255], off offset:2560
	s_waitcnt vmcnt(0)
	v_mfma_f32_32x32x16_f16 v[232:247], v[200:203], v[136:139], v[232:247]
	v_mfma_f32_32x32x16_f16 v[232:247], v[204:207], v[128:131], v[232:247]
	v_mfma_f32_32x32x16_f16 v[232:247], v[208:211], v[120:123], v[232:247]
	v_mfma_f32_32x32x16_f16 v[232:247], v[212:215], v[112:115], v[232:247]
	s_nop 15
	s_nop 3
	v_max3_f32 v248, v216, v217, v218
	v_max3_f32 v249, v219, v220, v221
	v_max3_f32 v248, v248, v222, v223
	v_max3_f32 v249, v249, v224, v225
	v_max3_f32 v248, v248, v226, v227
	v_max3_f32 v249, v249, v228, v229
	v_max3_f32 v248, v248, v230, v231
	v_max3_f32 v249, v249, v232, v233
	v_max3_f32 v248, v248, v234, v235
	v_max3_f32 v249, v249, v236, v237
	v_max3_f32 v248, v248, v238, v239
	v_max3_f32 v249, v249, v240, v241
	v_max3_f32 v248, v248, v242, v243
	v_max3_f32 v249, v249, v244, v245
	v_max3_f32 v248, v248, v246, v247
	v_max_f32_e32 v248, v248, v249
	v_mov_b32_e32 v249, v248
	s_nop 1
	v_permlane32_swap_b32_e32 v248, v249
	v_max_f32_e32 v248, v249, v248
	s_mov_b32 s37, 0x41000000
	v_cmp_lt_f32_e32 vcc, s37, v248
	s_nop 4
	s_cbranch_vccz .Lmy_rare_1_nr
	v_max_f32_e32 v248, 0, v248
	v_add_f32_e32 v194, v194, v248
	v_exp_f32_e64 v249, -v248
	v_sub_f32_e32 v216, v216, v248
	v_sub_f32_e32 v217, v217, v248
	v_sub_f32_e32 v218, v218, v248
	v_sub_f32_e32 v219, v219, v248
	v_sub_f32_e32 v220, v220, v248
	v_sub_f32_e32 v221, v221, v248
	v_sub_f32_e32 v222, v222, v248
	v_sub_f32_e32 v223, v223, v248
	v_sub_f32_e32 v224, v224, v248
	v_sub_f32_e32 v225, v225, v248
	v_sub_f32_e32 v226, v226, v248
	v_sub_f32_e32 v227, v227, v248
	v_sub_f32_e32 v228, v228, v248
	v_sub_f32_e32 v229, v229, v248
	v_sub_f32_e32 v230, v230, v248
	v_sub_f32_e32 v231, v231, v248
	v_sub_f32_e32 v232, v232, v248
	v_sub_f32_e32 v233, v233, v248
	v_sub_f32_e32 v234, v234, v248
	v_sub_f32_e32 v235, v235, v248
	v_sub_f32_e32 v236, v236, v248
	v_sub_f32_e32 v237, v237, v248
	v_sub_f32_e32 v238, v238, v248
	v_sub_f32_e32 v239, v239, v248
	v_sub_f32_e32 v240, v240, v248
	v_sub_f32_e32 v241, v241, v248
	v_sub_f32_e32 v242, v242, v248
	v_sub_f32_e32 v243, v243, v248
	v_sub_f32_e32 v244, v244, v248
	v_sub_f32_e32 v245, v245, v248
	v_sub_f32_e32 v246, v246, v248
	v_sub_f32_e32 v247, v247, v248
	v_sub_f32_e32 v96, v96, v248
	v_sub_f32_e32 v97, v97, v248
	v_sub_f32_e32 v98, v98, v248
	v_sub_f32_e32 v99, v99, v248
	v_sub_f32_e32 v100, v100, v248
	v_sub_f32_e32 v101, v101, v248
	v_sub_f32_e32 v102, v102, v248
	v_sub_f32_e32 v103, v103, v248
	v_sub_f32_e32 v104, v104, v248
	v_sub_f32_e32 v105, v105, v248
	v_sub_f32_e32 v106, v106, v248
	v_sub_f32_e32 v107, v107, v248
	v_sub_f32_e32 v108, v108, v248
	v_sub_f32_e32 v109, v109, v248
	v_sub_f32_e32 v110, v110, v248
	v_sub_f32_e32 v111, v111, v248
	v_sub_f32_e32 v80, v80, v248
	v_sub_f32_e32 v81, v81, v248
	v_sub_f32_e32 v82, v82, v248
	v_sub_f32_e32 v83, v83, v248
	v_sub_f32_e32 v84, v84, v248
	v_sub_f32_e32 v85, v85, v248
	v_sub_f32_e32 v86, v86, v248
	v_sub_f32_e32 v87, v87, v248
	v_sub_f32_e32 v88, v88, v248
	v_sub_f32_e32 v89, v89, v248
	v_sub_f32_e32 v90, v90, v248
	v_sub_f32_e32 v91, v91, v248
	v_sub_f32_e32 v92, v92, v248
	v_sub_f32_e32 v93, v93, v248
	v_sub_f32_e32 v94, v94, v248
	v_sub_f32_e32 v95, v95, v248
	v_xor_b32_e32 v0, 0x80000000, v194
	v_mov_b32_e32 v1, v0
	v_mov_b32_e32 v2, v0
	v_mov_b32_e32 v3, v0
	v_mov_b32_e32 v4, v0
	v_mov_b32_e32 v5, v0
	v_mov_b32_e32 v6, v0
	v_mov_b32_e32 v7, v0
	v_mov_b32_e32 v8, v0
	v_mov_b32_e32 v9, v0
	v_mov_b32_e32 v10, v0
	v_mov_b32_e32 v11, v0
	v_mov_b32_e32 v12, v0
	v_mov_b32_e32 v13, v0
	v_mov_b32_e32 v14, v0
	v_mov_b32_e32 v15, v0
	v_mul_f32_e32 v187, v187, v249
	s_and_saveexec_b64 s[40:41], s[0:1]
	ds_write_b32 v186, v249 offset:57344
	s_or_b64 exec, exec, s[40:41]
	v_add_u32_e32 v250, s11, v193
	s_waitcnt lgkmcnt(0)
	ds_read_b128 v[200:203], v250 offset:57344
	ds_read_b128 v[204:207], v250 offset:57376
	ds_read_b128 v[208:211], v250 offset:57408
	ds_read_b128 v[212:215], v250 offset:57440
	s_waitcnt lgkmcnt(0)
	v_pk_mul_f32 v[16:17], v[16:17], v[200:201]
	v_pk_mul_f32 v[32:33], v[32:33], v[200:201]
	v_pk_mul_f32 v[18:19], v[18:19], v[202:203]
	v_pk_mul_f32 v[34:35], v[34:35], v[202:203]
	v_pk_mul_f32 v[20:21], v[20:21], v[204:205]
	v_pk_mul_f32 v[36:37], v[36:37], v[204:205]
	v_pk_mul_f32 v[22:23], v[22:23], v[206:207]
	v_pk_mul_f32 v[38:39], v[38:39], v[206:207]
	v_pk_mul_f32 v[24:25], v[24:25], v[208:209]
	v_pk_mul_f32 v[40:41], v[40:41], v[208:209]
	v_pk_mul_f32 v[26:27], v[26:27], v[210:211]
	v_pk_mul_f32 v[42:43], v[42:43], v[210:211]
	v_pk_mul_f32 v[28:29], v[28:29], v[212:213]
	v_pk_mul_f32 v[44:45], v[44:45], v[212:213]
	v_pk_mul_f32 v[30:31], v[30:31], v[214:215]
	v_pk_mul_f32 v[46:47], v[46:47], v[214:215]
.Lmy_rare_1_nr:
	v_exp_f32_e32 v216, v216
	v_exp_f32_e32 v217, v217
	v_exp_f32_e32 v218, v218
	v_exp_f32_e32 v219, v219
	v_exp_f32_e32 v220, v220
	v_exp_f32_e32 v221, v221
	v_exp_f32_e32 v222, v222
	v_exp_f32_e32 v223, v223
	v_exp_f32_e32 v224, v224
	v_exp_f32_e32 v225, v225
	v_exp_f32_e32 v226, v226
	v_exp_f32_e32 v227, v227
	v_exp_f32_e32 v228, v228
	v_exp_f32_e32 v229, v229
	v_exp_f32_e32 v230, v230
	v_exp_f32_e32 v231, v231
	v_exp_f32_e32 v232, v232
	v_exp_f32_e32 v233, v233
	v_exp_f32_e32 v234, v234
	v_exp_f32_e32 v235, v235
	v_exp_f32_e32 v236, v236
	v_exp_f32_e32 v237, v237
	v_exp_f32_e32 v238, v238
	v_exp_f32_e32 v239, v239
	v_exp_f32_e32 v240, v240
	v_exp_f32_e32 v241, v241
	v_exp_f32_e32 v242, v242
	v_exp_f32_e32 v243, v243
	v_exp_f32_e32 v244, v244
	v_exp_f32_e32 v245, v245
	v_exp_f32_e32 v246, v246
	v_exp_f32_e32 v247, v247
	s_nop 0
	v_cvt_pk_f16_f32 v140, v216, v217
	v_cvt_pk_f16_f32 v141, v218, v219
	v_cvt_pk_f16_f32 v142, v220, v221
	v_cvt_pk_f16_f32 v143, v222, v223
	v_cvt_pk_f16_f32 v132, v224, v225
	v_cvt_pk_f16_f32 v133, v226, v227
	v_cvt_pk_f16_f32 v134, v228, v229
	v_cvt_pk_f16_f32 v135, v230, v231
	v_cvt_pk_f16_f32 v124, v232, v233
	v_cvt_pk_f16_f32 v125, v234, v235
	v_cvt_pk_f16_f32 v126, v236, v237
	v_cvt_pk_f16_f32 v127, v238, v239
	v_cvt_pk_f16_f32 v116, v240, v241
	v_cvt_pk_f16_f32 v117, v242, v243
	v_cvt_pk_f16_f32 v118, v244, v245
	v_cvt_pk_f16_f32 v119, v246, v247
	v_add_f32_e32 v76, v216, v217
	v_add_f32_e32 v76, v218, v76
	v_add_f32_e32 v76, v219, v76
	v_add_f32_e32 v76, v220, v76
	v_add_f32_e32 v76, v221, v76
	v_add_f32_e32 v76, v222, v76
	v_add_f32_e32 v76, v223, v76
	v_add_f32_e32 v76, v224, v76
	v_add_f32_e32 v76, v225, v76
	v_add_f32_e32 v76, v226, v76
	v_add_f32_e32 v76, v227, v76
	v_add_f32_e32 v76, v228, v76
	v_add_f32_e32 v76, v229, v76
	v_add_f32_e32 v76, v230, v76
	v_add_f32_e32 v76, v231, v76
	v_add_f32_e32 v76, v232, v76
	v_add_f32_e32 v76, v233, v76
	v_add_f32_e32 v76, v234, v76
	v_add_f32_e32 v76, v235, v76
	v_add_f32_e32 v76, v236, v76
	v_add_f32_e32 v76, v237, v76
	v_add_f32_e32 v76, v238, v76
	v_add_f32_e32 v76, v239, v76
	v_add_f32_e32 v76, v240, v76
	v_add_f32_e32 v76, v241, v76
	v_add_f32_e32 v76, v242, v76
	v_add_f32_e32 v76, v243, v76
	v_add_f32_e32 v76, v244, v76
	v_add_f32_e32 v76, v245, v76
	v_add_f32_e32 v76, v246, v76
	v_add_f32_e32 v76, v247, v76
	s_branch .Lmy_back_1
.Lmy_rare_2:
	v_subrev_u32_e32 v248, s25, v191
	v_ashrrev_i32_e32 v249, 31, v248
	v_lshl_add_u64 v[250:251], v[182:183], 0, v[248:249]
	s_mov_b64 s[38:39], 0x1000
	v_lshl_add_u64 v[254:255], v[250:251], 0, s[38:39]
	v_xor_b32_e32 v252, 0x80000000, v194
	global_load_dwordx4 v[200:203], v[250:251], off
	global_load_dwordx4 v[204:207], v[250:251], off offset:2048
	global_load_dwordx4 v[208:211], v[254:255], off
	global_load_dwordx4 v[212:215], v[254:255], off offset:2048
	v_mov_b32_e32 v216, v252
	v_mov_b32_e32 v217, v252
	v_mov_b32_e32 v218, v252
	v_mov_b32_e32 v219, v252
	v_mov_b32_e32 v220, v252
	v_mov_b32_e32 v221, v252
	v_mov_b32_e32 v222, v252
	v_mov_b32_e32 v223, v252
	v_mov_b32_e32 v224, v252
	v_mov_b32_e32 v225, v252
	v_mov_b32_e32 v226, v252
	v_mov_b32_e32 v227, v252
	v_mov_b32_e32 v228, v252
	v_mov_b32_e32 v229, v252
	v_mov_b32_e32 v230, v252
	v_mov_b32_e32 v231, v252
	v_mov_b32_e32 v232, v252
	v_mov_b32_e32 v233, v252
	v_mov_b32_e32 v234, v252
	v_mov_b32_e32 v235, v252
	v_mov_b32_e32 v236, v252
	v_mov_b32_e32 v237, v252
	v_mov_b32_e32 v238, v252
	v_mov_b32_e32 v239, v252
	v_mov_b32_e32 v240, v252
	v_mov_b32_e32 v241, v252
	v_mov_b32_e32 v242, v252
	v_mov_b32_e32 v243, v252
	v_mov_b32_e32 v244, v252
	v_mov_b32_e32 v245, v252
	v_mov_b32_e32 v246, v252
	v_mov_b32_e32 v247, v252
	s_waitcnt vmcnt(0)
	v_mfma_f32_32x32x16_f16 v[216:231], v[200:203], v[136:139], v[216:231]
	v_mfma_f32_32x32x16_f16 v[216:231], v[204:207], v[128:131], v[216:231]
	v_mfma_f32_32x32x16_f16 v[216:231], v[208:211], v[120:123], v[216:231]
	v_mfma_f32_32x32x16_f16 v[216:231], v[212:215], v[112:115], v[216:231]
	global_load_dwordx4 v[200:203], v[250:251], off offset:512
	global_load_dwordx4 v[204:207], v[250:251], off offset:2560
	global_load_dwordx4 v[208:211], v[254:255], off offset:512
	global_load_dwordx4 v[212:215], v[254:255], off offset:2560
	s_waitcnt vmcnt(0)
	v_mfma_f32_32x32x16_f16 v[232:247], v[200:203], v[136:139], v[232:247]
	v_mfma_f32_32x32x16_f16 v[232:247], v[204:207], v[128:131], v[232:247]
	v_mfma_f32_32x32x16_f16 v[232:247], v[208:211], v[120:123], v[232:247]
	v_mfma_f32_32x32x16_f16 v[232:247], v[212:215], v[112:115], v[232:247]
	s_nop 15
	s_nop 3
	v_max3_f32 v248, v216, v217, v218
	v_max3_f32 v249, v219, v220, v221
	v_max3_f32 v248, v248, v222, v223
	v_max3_f32 v249, v249, v224, v225
	v_max3_f32 v248, v248, v226, v227
	v_max3_f32 v249, v249, v228, v229
	v_max3_f32 v248, v248, v230, v231
	v_max3_f32 v249, v249, v232, v233
	v_max3_f32 v248, v248, v234, v235
	v_max3_f32 v249, v249, v236, v237
	v_max3_f32 v248, v248, v238, v239
	v_max3_f32 v249, v249, v240, v241
	v_max3_f32 v248, v248, v242, v243
	v_max3_f32 v249, v249, v244, v245
	v_max3_f32 v248, v248, v246, v247
	v_max_f32_e32 v248, v248, v249
	v_mov_b32_e32 v249, v248
	s_nop 1
	v_permlane32_swap_b32_e32 v248, v249
	v_max_f32_e32 v248, v249, v248
	s_mov_b32 s37, 0x41000000
	v_cmp_lt_f32_e32 vcc, s37, v248
	s_nop 4
	s_cbranch_vccz .Lmy_rare_2_nr
	v_max_f32_e32 v248, 0, v248
	v_add_f32_e32 v194, v194, v248
	v_exp_f32_e64 v249, -v248
	v_sub_f32_e32 v216, v216, v248
	v_sub_f32_e32 v217, v217, v248
	v_sub_f32_e32 v218, v218, v248
	v_sub_f32_e32 v219, v219, v248
	v_sub_f32_e32 v220, v220, v248
	v_sub_f32_e32 v221, v221, v248
	v_sub_f32_e32 v222, v222, v248
	v_sub_f32_e32 v223, v223, v248
	v_sub_f32_e32 v224, v224, v248
	v_sub_f32_e32 v225, v225, v248
	v_sub_f32_e32 v226, v226, v248
	v_sub_f32_e32 v227, v227, v248
	v_sub_f32_e32 v228, v228, v248
	v_sub_f32_e32 v229, v229, v248
	v_sub_f32_e32 v230, v230, v248
	v_sub_f32_e32 v231, v231, v248
	v_sub_f32_e32 v232, v232, v248
	v_sub_f32_e32 v233, v233, v248
	v_sub_f32_e32 v234, v234, v248
	v_sub_f32_e32 v235, v235, v248
	v_sub_f32_e32 v236, v236, v248
	v_sub_f32_e32 v237, v237, v248
	v_sub_f32_e32 v238, v238, v248
	v_sub_f32_e32 v239, v239, v248
	v_sub_f32_e32 v240, v240, v248
	v_sub_f32_e32 v241, v241, v248
	v_sub_f32_e32 v242, v242, v248
	v_sub_f32_e32 v243, v243, v248
	v_sub_f32_e32 v244, v244, v248
	v_sub_f32_e32 v245, v245, v248
	v_sub_f32_e32 v246, v246, v248
	v_sub_f32_e32 v247, v247, v248
	v_sub_f32_e32 v64, v64, v248
	v_sub_f32_e32 v65, v65, v248
	v_sub_f32_e32 v66, v66, v248
	v_sub_f32_e32 v67, v67, v248
	v_sub_f32_e32 v68, v68, v248
	v_sub_f32_e32 v69, v69, v248
	v_sub_f32_e32 v70, v70, v248
	v_sub_f32_e32 v71, v71, v248
	v_sub_f32_e32 v72, v72, v248
	v_sub_f32_e32 v73, v73, v248
	v_sub_f32_e32 v74, v74, v248
	v_sub_f32_e32 v75, v75, v248
	v_sub_f32_e32 v76, v76, v248
	v_sub_f32_e32 v77, v77, v248
	v_sub_f32_e32 v78, v78, v248
	v_sub_f32_e32 v79, v79, v248
	v_sub_f32_e32 v48, v48, v248
	v_sub_f32_e32 v49, v49, v248
	v_sub_f32_e32 v50, v50, v248
	v_sub_f32_e32 v51, v51, v248
	v_sub_f32_e32 v52, v52, v248
	v_sub_f32_e32 v53, v53, v248
	v_sub_f32_e32 v54, v54, v248
	v_sub_f32_e32 v55, v55, v248
	v_sub_f32_e32 v56, v56, v248
	v_sub_f32_e32 v57, v57, v248
	v_sub_f32_e32 v58, v58, v248
	v_sub_f32_e32 v59, v59, v248
	v_sub_f32_e32 v60, v60, v248
	v_sub_f32_e32 v61, v61, v248
	v_sub_f32_e32 v62, v62, v248
	v_sub_f32_e32 v63, v63, v248
	v_xor_b32_e32 v0, 0x80000000, v194
	v_mov_b32_e32 v1, v0
	v_mov_b32_e32 v2, v0
	v_mov_b32_e32 v3, v0
	v_mov_b32_e32 v4, v0
	v_mov_b32_e32 v5, v0
	v_mov_b32_e32 v6, v0
	v_mov_b32_e32 v7, v0
	v_mov_b32_e32 v8, v0
	v_mov_b32_e32 v9, v0
	v_mov_b32_e32 v10, v0
	v_mov_b32_e32 v11, v0
	v_mov_b32_e32 v12, v0
	v_mov_b32_e32 v13, v0
	v_mov_b32_e32 v14, v0
	v_mov_b32_e32 v15, v0
	v_mul_f32_e32 v187, v187, v249
	s_and_saveexec_b64 s[40:41], s[0:1]
	ds_write_b32 v186, v249 offset:57344
	s_or_b64 exec, exec, s[40:41]
	v_add_u32_e32 v250, s11, v193
	s_waitcnt lgkmcnt(0)
	ds_read_b128 v[200:203], v250 offset:57344
	ds_read_b128 v[204:207], v250 offset:57376
	ds_read_b128 v[208:211], v250 offset:57408
	ds_read_b128 v[212:215], v250 offset:57440
	s_waitcnt lgkmcnt(0)
	v_pk_mul_f32 v[16:17], v[16:17], v[200:201]
	v_pk_mul_f32 v[32:33], v[32:33], v[200:201]
	v_pk_mul_f32 v[18:19], v[18:19], v[202:203]
	v_pk_mul_f32 v[34:35], v[34:35], v[202:203]
	v_pk_mul_f32 v[20:21], v[20:21], v[204:205]
	v_pk_mul_f32 v[36:37], v[36:37], v[204:205]
	v_pk_mul_f32 v[22:23], v[22:23], v[206:207]
	v_pk_mul_f32 v[38:39], v[38:39], v[206:207]
	v_pk_mul_f32 v[24:25], v[24:25], v[208:209]
	v_pk_mul_f32 v[40:41], v[40:41], v[208:209]
	v_pk_mul_f32 v[26:27], v[26:27], v[210:211]
	v_pk_mul_f32 v[42:43], v[42:43], v[210:211]
	v_pk_mul_f32 v[28:29], v[28:29], v[212:213]
	v_pk_mul_f32 v[44:45], v[44:45], v[212:213]
	v_pk_mul_f32 v[30:31], v[30:31], v[214:215]
	v_pk_mul_f32 v[46:47], v[46:47], v[214:215]
.Lmy_rare_2_nr:
	v_exp_f32_e32 v216, v216
	v_exp_f32_e32 v217, v217
	v_exp_f32_e32 v218, v218
	v_exp_f32_e32 v219, v219
	v_exp_f32_e32 v220, v220
	v_exp_f32_e32 v221, v221
	v_exp_f32_e32 v222, v222
	v_exp_f32_e32 v223, v223
	v_exp_f32_e32 v224, v224
	v_exp_f32_e32 v225, v225
	v_exp_f32_e32 v226, v226
	v_exp_f32_e32 v227, v227
	v_exp_f32_e32 v228, v228
	v_exp_f32_e32 v229, v229
	v_exp_f32_e32 v230, v230
	v_exp_f32_e32 v231, v231
	v_exp_f32_e32 v232, v232
	v_exp_f32_e32 v233, v233
	v_exp_f32_e32 v234, v234
	v_exp_f32_e32 v235, v235
	v_exp_f32_e32 v236, v236
	v_exp_f32_e32 v237, v237
	v_exp_f32_e32 v238, v238
	v_exp_f32_e32 v239, v239
	v_exp_f32_e32 v240, v240
	v_exp_f32_e32 v241, v241
	v_exp_f32_e32 v242, v242
	v_exp_f32_e32 v243, v243
	v_exp_f32_e32 v244, v244
	v_exp_f32_e32 v245, v245
	v_exp_f32_e32 v246, v246
	v_exp_f32_e32 v247, v247
	s_nop 0
	v_cvt_pk_f16_f32 v140, v216, v217
	v_cvt_pk_f16_f32 v141, v218, v219
	v_cvt_pk_f16_f32 v142, v220, v221
	v_cvt_pk_f16_f32 v143, v222, v223
	v_cvt_pk_f16_f32 v132, v224, v225
	v_cvt_pk_f16_f32 v133, v226, v227
	v_cvt_pk_f16_f32 v134, v228, v229
	v_cvt_pk_f16_f32 v135, v230, v231
	v_cvt_pk_f16_f32 v124, v232, v233
	v_cvt_pk_f16_f32 v125, v234, v235
	v_cvt_pk_f16_f32 v126, v236, v237
	v_cvt_pk_f16_f32 v127, v238, v239
	v_cvt_pk_f16_f32 v116, v240, v241
	v_cvt_pk_f16_f32 v117, v242, v243
	v_cvt_pk_f16_f32 v118, v244, v245
	v_cvt_pk_f16_f32 v119, v246, v247
	v_add_f32_e32 v104, v216, v217
	v_add_f32_e32 v104, v218, v104
	v_add_f32_e32 v104, v219, v104
	v_add_f32_e32 v104, v220, v104
	v_add_f32_e32 v104, v221, v104
	v_add_f32_e32 v104, v222, v104
	v_add_f32_e32 v104, v223, v104
	v_add_f32_e32 v104, v224, v104
	v_add_f32_e32 v104, v225, v104
	v_add_f32_e32 v104, v226, v104
	v_add_f32_e32 v104, v227, v104
	v_add_f32_e32 v104, v228, v104
	v_add_f32_e32 v104, v229, v104
	v_add_f32_e32 v104, v230, v104
	v_add_f32_e32 v104, v231, v104
	v_add_f32_e32 v104, v232, v104
	v_add_f32_e32 v104, v233, v104
	v_add_f32_e32 v104, v234, v104
	v_add_f32_e32 v104, v235, v104
	v_add_f32_e32 v104, v236, v104
	v_add_f32_e32 v104, v237, v104
	v_add_f32_e32 v104, v238, v104
	v_add_f32_e32 v104, v239, v104
	v_add_f32_e32 v104, v240, v104
	v_add_f32_e32 v104, v241, v104
	v_add_f32_e32 v104, v242, v104
	v_add_f32_e32 v104, v243, v104
	v_add_f32_e32 v104, v244, v104
	v_add_f32_e32 v104, v245, v104
	v_add_f32_e32 v104, v246, v104
	v_add_f32_e32 v104, v247, v104
	s_branch .Lmy_back_2
.Lmy_rare_3:
	v_subrev_u32_e32 v248, s25, v191
	v_add_u32_e32 v248, 0xffffe000, v248
	v_ashrrev_i32_e32 v249, 31, v248
	v_lshl_add_u64 v[250:251], v[182:183], 0, v[248:249]
	s_mov_b64 s[38:39], 0x1000
	v_lshl_add_u64 v[254:255], v[250:251], 0, s[38:39]
	v_xor_b32_e32 v252, 0x80000000, v194
	global_load_dwordx4 v[200:203], v[250:251], off
	global_load_dwordx4 v[204:207], v[250:251], off offset:2048
	global_load_dwordx4 v[208:211], v[254:255], off
	global_load_dwordx4 v[212:215], v[254:255], off offset:2048
	v_mov_b32_e32 v216, v252
	v_mov_b32_e32 v217, v252
	v_mov_b32_e32 v218, v252
	v_mov_b32_e32 v219, v252
	v_mov_b32_e32 v220, v252
	v_mov_b32_e32 v221, v252
	v_mov_b32_e32 v222, v252
	v_mov_b32_e32 v223, v252
	v_mov_b32_e32 v224, v252
	v_mov_b32_e32 v225, v252
	v_mov_b32_e32 v226, v252
	v_mov_b32_e32 v227, v252
	v_mov_b32_e32 v228, v252
	v_mov_b32_e32 v229, v252
	v_mov_b32_e32 v230, v252
	v_mov_b32_e32 v231, v252
	v_mov_b32_e32 v232, v252
	v_mov_b32_e32 v233, v252
	v_mov_b32_e32 v234, v252
	v_mov_b32_e32 v235, v252
	v_mov_b32_e32 v236, v252
	v_mov_b32_e32 v237, v252
	v_mov_b32_e32 v238, v252
	v_mov_b32_e32 v239, v252
	v_mov_b32_e32 v240, v252
	v_mov_b32_e32 v241, v252
	v_mov_b32_e32 v242, v252
	v_mov_b32_e32 v243, v252
	v_mov_b32_e32 v244, v252
	v_mov_b32_e32 v245, v252
	v_mov_b32_e32 v246, v252
	v_mov_b32_e32 v247, v252
	s_waitcnt vmcnt(0)
	v_mfma_f32_32x32x16_f16 v[216:231], v[200:203], v[136:139], v[216:231]
	v_mfma_f32_32x32x16_f16 v[216:231], v[204:207], v[128:131], v[216:231]
	v_mfma_f32_32x32x16_f16 v[216:231], v[208:211], v[120:123], v[216:231]
	v_mfma_f32_32x32x16_f16 v[216:231], v[212:215], v[112:115], v[216:231]
	global_load_dwordx4 v[200:203], v[250:251], off offset:512
	global_load_dwordx4 v[204:207], v[250:251], off offset:2560
	global_load_dwordx4 v[208:211], v[254:255], off offset:512
	global_load_dwordx4 v[212:215], v[254:255], off offset:2560
	s_waitcnt vmcnt(0)
	v_mfma_f32_32x32x16_f16 v[232:247], v[200:203], v[136:139], v[232:247]
	v_mfma_f32_32x32x16_f16 v[232:247], v[204:207], v[128:131], v[232:247]
	v_mfma_f32_32x32x16_f16 v[232:247], v[208:211], v[120:123], v[232:247]
	v_mfma_f32_32x32x16_f16 v[232:247], v[212:215], v[112:115], v[232:247]
	s_nop 15
	s_nop 3
	v_max3_f32 v248, v216, v217, v218
	v_max3_f32 v249, v219, v220, v221
	v_max3_f32 v248, v248, v222, v223
	v_max3_f32 v249, v249, v224, v225
	v_max3_f32 v248, v248, v226, v227
	v_max3_f32 v249, v249, v228, v229
	v_max3_f32 v248, v248, v230, v231
	v_max3_f32 v249, v249, v232, v233
	v_max3_f32 v248, v248, v234, v235
	v_max3_f32 v249, v249, v236, v237
	v_max3_f32 v248, v248, v238, v239
	v_max3_f32 v249, v249, v240, v241
	v_max3_f32 v248, v248, v242, v243
	v_max3_f32 v249, v249, v244, v245
	v_max3_f32 v248, v248, v246, v247
	v_max_f32_e32 v248, v248, v249
	v_mov_b32_e32 v249, v248
	s_nop 1
	v_permlane32_swap_b32_e32 v248, v249
	v_max_f32_e32 v248, v249, v248
	s_mov_b32 s37, 0x41000000
	v_cmp_lt_f32_e32 vcc, s37, v248
	s_nop 4
	s_cbranch_vccz .Lmy_rare_3_nr
	v_max_f32_e32 v248, 0, v248
	v_add_f32_e32 v194, v194, v248
	v_exp_f32_e64 v249, -v248
	v_sub_f32_e32 v216, v216, v248
	v_sub_f32_e32 v217, v217, v248
	v_sub_f32_e32 v218, v218, v248
	v_sub_f32_e32 v219, v219, v248
	v_sub_f32_e32 v220, v220, v248
	v_sub_f32_e32 v221, v221, v248
	v_sub_f32_e32 v222, v222, v248
	v_sub_f32_e32 v223, v223, v248
	v_sub_f32_e32 v224, v224, v248
	v_sub_f32_e32 v225, v225, v248
	v_sub_f32_e32 v226, v226, v248
	v_sub_f32_e32 v227, v227, v248
	v_sub_f32_e32 v228, v228, v248
	v_sub_f32_e32 v229, v229, v248
	v_sub_f32_e32 v230, v230, v248
	v_sub_f32_e32 v231, v231, v248
	v_sub_f32_e32 v232, v232, v248
	v_sub_f32_e32 v233, v233, v248
	v_sub_f32_e32 v234, v234, v248
	v_sub_f32_e32 v235, v235, v248
	v_sub_f32_e32 v236, v236, v248
	v_sub_f32_e32 v237, v237, v248
	v_sub_f32_e32 v238, v238, v248
	v_sub_f32_e32 v239, v239, v248
	v_sub_f32_e32 v240, v240, v248
	v_sub_f32_e32 v241, v241, v248
	v_sub_f32_e32 v242, v242, v248
	v_sub_f32_e32 v243, v243, v248
	v_sub_f32_e32 v244, v244, v248
	v_sub_f32_e32 v245, v245, v248
	v_sub_f32_e32 v246, v246, v248
	v_sub_f32_e32 v247, v247, v248
	v_sub_f32_e32 v80, v80, v248
	v_sub_f32_e32 v81, v81, v248
	v_sub_f32_e32 v82, v82, v248
	v_sub_f32_e32 v83, v83, v248
	v_sub_f32_e32 v84, v84, v248
	v_sub_f32_e32 v85, v85, v248
	v_sub_f32_e32 v86, v86, v248
	v_sub_f32_e32 v87, v87, v248
	v_sub_f32_e32 v88, v88, v248
	v_sub_f32_e32 v89, v89, v248
	v_sub_f32_e32 v90, v90, v248
	v_sub_f32_e32 v91, v91, v248
	v_sub_f32_e32 v92, v92, v248
	v_sub_f32_e32 v93, v93, v248
	v_sub_f32_e32 v94, v94, v248
	v_sub_f32_e32 v95, v95, v248
	v_sub_f32_e32 v0, v0, v248
	v_sub_f32_e32 v1, v1, v248
	v_sub_f32_e32 v2, v2, v248
	v_sub_f32_e32 v3, v3, v248
	v_sub_f32_e32 v4, v4, v248
	v_sub_f32_e32 v5, v5, v248
	v_sub_f32_e32 v6, v6, v248
	v_sub_f32_e32 v7, v7, v248
	v_sub_f32_e32 v8, v8, v248
	v_sub_f32_e32 v9, v9, v248
	v_sub_f32_e32 v10, v10, v248
	v_sub_f32_e32 v11, v11, v248
	v_sub_f32_e32 v12, v12, v248
	v_sub_f32_e32 v13, v13, v248
	v_sub_f32_e32 v14, v14, v248
	v_sub_f32_e32 v15, v15, v248
	v_mul_f32_e32 v187, v187, v249
	s_and_saveexec_b64 s[40:41], s[0:1]
	ds_write_b32 v186, v249 offset:57344
	s_or_b64 exec, exec, s[40:41]
	v_add_u32_e32 v250, s11, v193
	s_waitcnt lgkmcnt(0)
	ds_read_b128 v[200:203], v250 offset:57344
	ds_read_b128 v[204:207], v250 offset:57376
	ds_read_b128 v[208:211], v250 offset:57408
	ds_read_b128 v[212:215], v250 offset:57440
	s_waitcnt lgkmcnt(0)
	v_pk_mul_f32 v[16:17], v[16:17], v[200:201]
	v_pk_mul_f32 v[32:33], v[32:33], v[200:201]
	v_pk_mul_f32 v[18:19], v[18:19], v[202:203]
	v_pk_mul_f32 v[34:35], v[34:35], v[202:203]
	v_pk_mul_f32 v[20:21], v[20:21], v[204:205]
	v_pk_mul_f32 v[36:37], v[36:37], v[204:205]
	v_pk_mul_f32 v[22:23], v[22:23], v[206:207]
	v_pk_mul_f32 v[38:39], v[38:39], v[206:207]
	v_pk_mul_f32 v[24:25], v[24:25], v[208:209]
	v_pk_mul_f32 v[40:41], v[40:41], v[208:209]
	v_pk_mul_f32 v[26:27], v[26:27], v[210:211]
	v_pk_mul_f32 v[42:43], v[42:43], v[210:211]
	v_pk_mul_f32 v[28:29], v[28:29], v[212:213]
	v_pk_mul_f32 v[44:45], v[44:45], v[212:213]
	v_pk_mul_f32 v[30:31], v[30:31], v[214:215]
	v_pk_mul_f32 v[46:47], v[46:47], v[214:215]
.Lmy_rare_3_nr:
	v_exp_f32_e32 v216, v216
	v_exp_f32_e32 v217, v217
	v_exp_f32_e32 v218, v218
	v_exp_f32_e32 v219, v219
	v_exp_f32_e32 v220, v220
	v_exp_f32_e32 v221, v221
	v_exp_f32_e32 v222, v222
	v_exp_f32_e32 v223, v223
	v_exp_f32_e32 v224, v224
	v_exp_f32_e32 v225, v225
	v_exp_f32_e32 v226, v226
	v_exp_f32_e32 v227, v227
	v_exp_f32_e32 v228, v228
	v_exp_f32_e32 v229, v229
	v_exp_f32_e32 v230, v230
	v_exp_f32_e32 v231, v231
	v_exp_f32_e32 v232, v232
	v_exp_f32_e32 v233, v233
	v_exp_f32_e32 v234, v234
	v_exp_f32_e32 v235, v235
	v_exp_f32_e32 v236, v236
	v_exp_f32_e32 v237, v237
	v_exp_f32_e32 v238, v238
	v_exp_f32_e32 v239, v239
	v_exp_f32_e32 v240, v240
	v_exp_f32_e32 v241, v241
	v_exp_f32_e32 v242, v242
	v_exp_f32_e32 v243, v243
	v_exp_f32_e32 v244, v244
	v_exp_f32_e32 v245, v245
	v_exp_f32_e32 v246, v246
	v_exp_f32_e32 v247, v247
	s_nop 0
	v_cvt_pk_f16_f32 v140, v216, v217
	v_cvt_pk_f16_f32 v141, v218, v219
	v_cvt_pk_f16_f32 v142, v220, v221
	v_cvt_pk_f16_f32 v143, v222, v223
	v_cvt_pk_f16_f32 v132, v224, v225
	v_cvt_pk_f16_f32 v133, v226, v227
	v_cvt_pk_f16_f32 v134, v228, v229
	v_cvt_pk_f16_f32 v135, v230, v231
	v_cvt_pk_f16_f32 v124, v232, v233
	v_cvt_pk_f16_f32 v125, v234, v235
	v_cvt_pk_f16_f32 v126, v236, v237
	v_cvt_pk_f16_f32 v127, v238, v239
	v_cvt_pk_f16_f32 v116, v240, v241
	v_cvt_pk_f16_f32 v117, v242, v243
	v_cvt_pk_f16_f32 v118, v244, v245
	v_cvt_pk_f16_f32 v119, v246, v247
	v_add_f32_e32 v48, v216, v217
	v_add_f32_e32 v48, v218, v48
	v_add_f32_e32 v48, v219, v48
	v_add_f32_e32 v48, v220, v48
	v_add_f32_e32 v48, v221, v48
	v_add_f32_e32 v48, v222, v48
	v_add_f32_e32 v48, v223, v48
	v_add_f32_e32 v48, v224, v48
	v_add_f32_e32 v48, v225, v48
	v_add_f32_e32 v48, v226, v48
	v_add_f32_e32 v48, v227, v48
	v_add_f32_e32 v48, v228, v48
	v_add_f32_e32 v48, v229, v48
	v_add_f32_e32 v48, v230, v48
	v_add_f32_e32 v48, v231, v48
	v_add_f32_e32 v48, v232, v48
	v_add_f32_e32 v48, v233, v48
	v_add_f32_e32 v48, v234, v48
	v_add_f32_e32 v48, v235, v48
	v_add_f32_e32 v48, v236, v48
	v_add_f32_e32 v48, v237, v48
	v_add_f32_e32 v48, v238, v48
	v_add_f32_e32 v48, v239, v48
	v_add_f32_e32 v48, v240, v48
	v_add_f32_e32 v48, v241, v48
	v_add_f32_e32 v48, v242, v48
	v_add_f32_e32 v48, v243, v48
	v_add_f32_e32 v48, v244, v48
	v_add_f32_e32 v48, v245, v48
	v_add_f32_e32 v48, v246, v48
	v_add_f32_e32 v48, v247, v48
	s_branch .Lmy_back_3
.Lmy_rare_4:
	v_subrev_u32_e32 v248, s25, v191
	v_ashrrev_i32_e32 v249, 31, v248
	v_lshl_add_u64 v[250:251], v[182:183], 0, v[248:249]
	s_mov_b64 s[38:39], 0x1000
	v_lshl_add_u64 v[254:255], v[250:251], 0, s[38:39]
	v_xor_b32_e32 v252, 0x80000000, v194
	global_load_dwordx4 v[200:203], v[250:251], off
	global_load_dwordx4 v[204:207], v[250:251], off offset:2048
	global_load_dwordx4 v[208:211], v[254:255], off
	global_load_dwordx4 v[212:215], v[254:255], off offset:2048
	v_mov_b32_e32 v216, v252
	v_mov_b32_e32 v217, v252
	v_mov_b32_e32 v218, v252
	v_mov_b32_e32 v219, v252
	v_mov_b32_e32 v220, v252
	v_mov_b32_e32 v221, v252
	v_mov_b32_e32 v222, v252
	v_mov_b32_e32 v223, v252
	v_mov_b32_e32 v224, v252
	v_mov_b32_e32 v225, v252
	v_mov_b32_e32 v226, v252
	v_mov_b32_e32 v227, v252
	v_mov_b32_e32 v228, v252
	v_mov_b32_e32 v229, v252
	v_mov_b32_e32 v230, v252
	v_mov_b32_e32 v231, v252
	v_mov_b32_e32 v232, v252
	v_mov_b32_e32 v233, v252
	v_mov_b32_e32 v234, v252
	v_mov_b32_e32 v235, v252
	v_mov_b32_e32 v236, v252
	v_mov_b32_e32 v237, v252
	v_mov_b32_e32 v238, v252
	v_mov_b32_e32 v239, v252
	v_mov_b32_e32 v240, v252
	v_mov_b32_e32 v241, v252
	v_mov_b32_e32 v242, v252
	v_mov_b32_e32 v243, v252
	v_mov_b32_e32 v244, v252
	v_mov_b32_e32 v245, v252
	v_mov_b32_e32 v246, v252
	v_mov_b32_e32 v247, v252
	s_waitcnt vmcnt(0)
	v_mfma_f32_32x32x16_f16 v[216:231], v[200:203], v[136:139], v[216:231]
	v_mfma_f32_32x32x16_f16 v[216:231], v[204:207], v[128:131], v[216:231]
	v_mfma_f32_32x32x16_f16 v[216:231], v[208:211], v[120:123], v[216:231]
	v_mfma_f32_32x32x16_f16 v[216:231], v[212:215], v[112:115], v[216:231]
	global_load_dwordx4 v[200:203], v[250:251], off offset:512
	global_load_dwordx4 v[204:207], v[250:251], off offset:2560
	global_load_dwordx4 v[208:211], v[254:255], off offset:512
	global_load_dwordx4 v[212:215], v[254:255], off offset:2560
	s_waitcnt vmcnt(0)
	v_mfma_f32_32x32x16_f16 v[232:247], v[200:203], v[136:139], v[232:247]
	v_mfma_f32_32x32x16_f16 v[232:247], v[204:207], v[128:131], v[232:247]
	v_mfma_f32_32x32x16_f16 v[232:247], v[208:211], v[120:123], v[232:247]
	v_mfma_f32_32x32x16_f16 v[232:247], v[212:215], v[112:115], v[232:247]
	s_nop 15
	s_nop 3
	v_max3_f32 v248, v216, v217, v218
	v_max3_f32 v249, v219, v220, v221
	v_max3_f32 v248, v248, v222, v223
	v_max3_f32 v249, v249, v224, v225
	v_max3_f32 v248, v248, v226, v227
	v_max3_f32 v249, v249, v228, v229
	v_max3_f32 v248, v248, v230, v231
	v_max3_f32 v249, v249, v232, v233
	v_max3_f32 v248, v248, v234, v235
	v_max3_f32 v249, v249, v236, v237
	v_max3_f32 v248, v248, v238, v239
	v_max3_f32 v249, v249, v240, v241
	v_max3_f32 v248, v248, v242, v243
	v_max3_f32 v249, v249, v244, v245
	v_max3_f32 v248, v248, v246, v247
	v_max_f32_e32 v248, v248, v249
	v_mov_b32_e32 v249, v248
	s_nop 1
	v_permlane32_swap_b32_e32 v248, v249
	v_max_f32_e32 v248, v249, v248
	s_mov_b32 s37, 0x41000000
	v_cmp_lt_f32_e32 vcc, s37, v248
	s_nop 4
	s_cbranch_vccz .Lmy_rare_4_nr
	v_max_f32_e32 v248, 0, v248
	v_add_f32_e32 v194, v194, v248
	v_exp_f32_e64 v249, -v248
	v_sub_f32_e32 v216, v216, v248
	v_sub_f32_e32 v217, v217, v248
	v_sub_f32_e32 v218, v218, v248
	v_sub_f32_e32 v219, v219, v248
	v_sub_f32_e32 v220, v220, v248
	v_sub_f32_e32 v221, v221, v248
	v_sub_f32_e32 v222, v222, v248
	v_sub_f32_e32 v223, v223, v248
	v_sub_f32_e32 v224, v224, v248
	v_sub_f32_e32 v225, v225, v248
	v_sub_f32_e32 v226, v226, v248
	v_sub_f32_e32 v227, v227, v248
	v_sub_f32_e32 v228, v228, v248
	v_sub_f32_e32 v229, v229, v248
	v_sub_f32_e32 v230, v230, v248
	v_sub_f32_e32 v231, v231, v248
	v_sub_f32_e32 v232, v232, v248
	v_sub_f32_e32 v233, v233, v248
	v_sub_f32_e32 v234, v234, v248
	v_sub_f32_e32 v235, v235, v248
	v_sub_f32_e32 v236, v236, v248
	v_sub_f32_e32 v237, v237, v248
	v_sub_f32_e32 v238, v238, v248
	v_sub_f32_e32 v239, v239, v248
	v_sub_f32_e32 v240, v240, v248
	v_sub_f32_e32 v241, v241, v248
	v_sub_f32_e32 v242, v242, v248
	v_sub_f32_e32 v243, v243, v248
	v_sub_f32_e32 v244, v244, v248
	v_sub_f32_e32 v245, v245, v248
	v_sub_f32_e32 v246, v246, v248
	v_sub_f32_e32 v247, v247, v248
	v_mul_f32_e32 v253, v253, v249
	s_and_saveexec_b64 s[40:41], s[0:1]
	ds_write_b32 v186, v249 offset:57344
	s_or_b64 exec, exec, s[40:41]
	v_add_u32_e32 v250, s11, v193
	s_waitcnt lgkmcnt(0)
	ds_read_b128 v[200:203], v250 offset:57344
	ds_read_b128 v[204:207], v250 offset:57376
	ds_read_b128 v[208:211], v250 offset:57408
	ds_read_b128 v[212:215], v250 offset:57440
	s_waitcnt lgkmcnt(0)
	v_pk_mul_f32 v[16:17], v[16:17], v[200:201]
	v_pk_mul_f32 v[32:33], v[32:33], v[200:201]
	v_pk_mul_f32 v[18:19], v[18:19], v[202:203]
	v_pk_mul_f32 v[34:35], v[34:35], v[202:203]
	v_pk_mul_f32 v[20:21], v[20:21], v[204:205]
	v_pk_mul_f32 v[36:37], v[36:37], v[204:205]
	v_pk_mul_f32 v[22:23], v[22:23], v[206:207]
	v_pk_mul_f32 v[38:39], v[38:39], v[206:207]
	v_pk_mul_f32 v[24:25], v[24:25], v[208:209]
	v_pk_mul_f32 v[40:41], v[40:41], v[208:209]
	v_pk_mul_f32 v[26:27], v[26:27], v[210:211]
	v_pk_mul_f32 v[42:43], v[42:43], v[210:211]
	v_pk_mul_f32 v[28:29], v[28:29], v[212:213]
	v_pk_mul_f32 v[44:45], v[44:45], v[212:213]
	v_pk_mul_f32 v[30:31], v[30:31], v[214:215]
	v_pk_mul_f32 v[46:47], v[46:47], v[214:215]
.Lmy_rare_4_nr:
	v_exp_f32_e32 v80, v216
	v_exp_f32_e32 v81, v217
	v_exp_f32_e32 v82, v218
	v_exp_f32_e32 v83, v219
	v_exp_f32_e32 v84, v220
	v_exp_f32_e32 v85, v221
	v_exp_f32_e32 v86, v222
	v_exp_f32_e32 v87, v223
	v_exp_f32_e32 v88, v224
	v_exp_f32_e32 v89, v225
	v_exp_f32_e32 v90, v226
	v_exp_f32_e32 v91, v227
	v_exp_f32_e32 v92, v228
	v_exp_f32_e32 v93, v229
	v_exp_f32_e32 v94, v230
	v_exp_f32_e32 v95, v231
	v_exp_f32_e32 v0, v232
	v_exp_f32_e32 v1, v233
	v_exp_f32_e32 v2, v234
	v_exp_f32_e32 v3, v235
	v_exp_f32_e32 v4, v236
	v_exp_f32_e32 v5, v237
	v_exp_f32_e32 v6, v238
	v_exp_f32_e32 v7, v239
	v_exp_f32_e32 v8, v240
	v_exp_f32_e32 v9, v241
	v_exp_f32_e32 v10, v242
	v_exp_f32_e32 v11, v243
	v_exp_f32_e32 v12, v244
	v_exp_f32_e32 v13, v245
	v_exp_f32_e32 v14, v246
	v_exp_f32_e32 v15, v247
	s_branch .Lmy_back_4

	.amdhsa_kernel _Z11attn_kernelPKDF16_S0_PDF16_
		.amdhsa_group_segment_fixed_size 0
		.amdhsa_private_segment_fixed_size 0
		.amdhsa_kernarg_size 24
		.amdhsa_user_sgpr_count 2
		.amdhsa_user_sgpr_dispatch_ptr 0
		.amdhsa_user_sgpr_queue_ptr 0
		.amdhsa_user_sgpr_kernarg_segment_ptr 1
		.amdhsa_user_sgpr_dispatch_id 0
		.amdhsa_user_sgpr_kernarg_preload_length 0
		.amdhsa_user_sgpr_kernarg_preload_offset 0
		.amdhsa_user_sgpr_private_segment_size 0
		.amdhsa_uses_dynamic_stack 0
		.amdhsa_enable_private_segment 0
		.amdhsa_system_sgpr_workgroup_id_x 1
		.amdhsa_system_sgpr_workgroup_id_y 0
		.amdhsa_system_sgpr_workgroup_id_z 0
		.amdhsa_system_sgpr_workgroup_info 0
		.amdhsa_system_vgpr_workitem_id 0
		.amdhsa_next_free_vgpr 256
		.amdhsa_next_free_sgpr 42
		.amdhsa_accum_offset 256
		.amdhsa_reserve_vcc 1
		.amdhsa_float_round_mode_32 0
		.amdhsa_float_round_mode_16_64 0
		.amdhsa_float_denorm_mode_32 3
		.amdhsa_float_denorm_mode_16_64 3
		.amdhsa_dx10_clamp 1
		.amdhsa_ieee_mode 1
		.amdhsa_fp16_overflow 0
		.amdhsa_tg_split 0
		.amdhsa_exception_fp_ieee_invalid_op 0
		.amdhsa_exception_fp_denorm_src 0
		.amdhsa_exception_fp_ieee_div_zero 0
		.amdhsa_exception_fp_ieee_overflow 0
		.amdhsa_exception_fp_ieee_underflow 0
		.amdhsa_exception_fp_ieee_inexact 0
		.amdhsa_exception_int_div_zero 0
	.end_amdhsa_kernel

amdhsa.kernels:
  - .agpr_count:     0
    .args:
      - .actual_access:  read_only
        .address_space:  global
        .offset:         0
        .size:           8
        .value_kind:     global_buffer
      - .actual_access:  read_only
        .address_space:  global
        .offset:         8
        .size:           8
        .value_kind:     global_buffer
      - .actual_access:  read_only
        .address_space:  global
        .offset:         16
        .size:           8
        .value_kind:     global_buffer
      - .actual_access:  read_only
        .address_space:  global
        .offset:         24
        .size:           8
        .value_kind:     global_buffer
      - .actual_access:  read_only
        .address_space:  global
        .offset:         32
        .size:           8
        .value_kind:     global_buffer
      - .actual_access:  write_only
        .address_space:  global
        .offset:         40
        .size:           8
        .value_kind:     global_buffer
      - .actual_access:  write_only
        .address_space:  global
        .offset:         48
        .size:           8
        .value_kind:     global_buffer
      - .actual_access:  write_only
        .address_space:  global
        .offset:         56
        .size:           8
        .value_kind:     global_buffer
      - .actual_access:  write_only
        .address_space:  global
        .offset:         64
        .size:           8
        .value_kind:     global_buffer
    .group_segment_fixed_size: 0
    .kernarg_segment_align: 8
    .kernarg_segment_size: 72
    .language:       OpenCL C
    .language_version:
      - 2
      - 0
    .max_flat_workgroup_size: 256
    .name:           _Z11prep_kernelPKfS0_S0_S0_S0_PDF16_S1_S1_S1_
    .private_segment_fixed_size: 0
    .sgpr_count:     21
    .sgpr_spill_count: 0
    .symbol:         _Z11prep_kernelPKfS0_S0_S0_S0_PDF16_S1_S1_S1_.kd
    .uniform_work_group_size: 1
    .uses_dynamic_stack: false
    .vgpr_count:     18
    .vgpr_spill_count: 0
    .wavefront_size: 64
  - .agpr_count:     0
    .args:
      - .actual_access:  read_only
        .address_space:  global
        .offset:         0
        .size:           8
        .value_kind:     global_buffer
      - .actual_access:  read_only
        .address_space:  global
        .offset:         8
        .size:           8
        .value_kind:     global_buffer
      - .actual_access:  read_only
        .address_space:  global
        .offset:         16
        .size:           8
        .value_kind:     global_buffer
      - .actual_access:  read_only
        .address_space:  global
        .offset:         24
        .size:           8
        .value_kind:     global_buffer
      - .actual_access:  read_only
        .address_space:  global
        .offset:         32
        .size:           8
        .value_kind:     global_buffer
      - .actual_access:  write_only
        .address_space:  global
        .offset:         40
        .size:           8
        .value_kind:     global_buffer
      - .actual_access:  write_only
        .address_space:  global
        .offset:         48
        .size:           8
        .value_kind:     global_buffer
    .group_segment_fixed_size: 0
    .kernarg_segment_align: 8
    .kernarg_segment_size: 56
    .language:       OpenCL C
    .language_version:
      - 2
      - 0
    .max_flat_workgroup_size: 512
    .name:           _Z11proj_kernelPKfS0_PKDF16_S0_S0_PDF16_S3_
    .private_segment_fixed_size: 0
    .sgpr_count:     21
    .sgpr_spill_count: 0
    .symbol:         _Z11proj_kernelPKfS0_PKDF16_S0_S0_PDF16_S3_.kd
    .uniform_work_group_size: 1
    .uses_dynamic_stack: false
    .vgpr_count:     170
    .vgpr_spill_count: 0
    .wavefront_size: 64
  - .agpr_count:     0
    .args:
      - .address_space:  global
        .offset:         0
        .size:           8
        .value_kind:     global_buffer
      - .address_space:  global
        .offset:         8
        .size:           8
        .value_kind:     global_buffer
      - .actual_access:  write_only
        .address_space:  global
        .offset:         16
        .size:           8
        .value_kind:     global_buffer
    .group_segment_fixed_size: 0
    .kernarg_segment_align: 8
    .kernarg_segment_size: 24
    .language:       OpenCL C
    .language_version:
      - 2
      - 0
    .max_flat_workgroup_size: 512
    .name:           _Z11attn_kernelPKDF16_S0_PDF16_
    .private_segment_fixed_size: 0
    .sgpr_count:     48
    .sgpr_spill_count: 0
    .symbol:         _Z11attn_kernelPKDF16_S0_PDF16_.kd
    .uniform_work_group_size: 1
    .uses_dynamic_stack: false
    .vgpr_count:     256
    .vgpr_spill_count: 0
    .wavefront_size: 64
  - .agpr_count:     0
    .args:
      - .actual_access:  read_only
        .address_space:  global
        .offset:         0
        .size:           8
        .value_kind:     global_buffer
      - .actual_access:  read_only
        .address_space:  global
        .offset:         8
        .size:           8
        .value_kind:     global_buffer
      - .actual_access:  read_only
        .address_space:  global
        .offset:         16
        .size:           8
        .value_kind:     global_buffer
      - .actual_access:  read_only
        .address_space:  global
        .offset:         24
        .size:           8
        .value_kind:     global_buffer
      - .actual_access:  read_only
        .address_space:  global
        .offset:         32
        .size:           8
        .value_kind:     global_buffer
      - .address_space:  global
        .offset:         40
        .size:           8
        .value_kind:     global_buffer
      - .actual_access:  read_only
        .address_space:  global
        .offset:         48
        .size:           8
        .value_kind:     global_buffer
      - .actual_access:  read_only
        .address_space:  global
        .offset:         56
        .size:           8
        .value_kind:     global_buffer
      - .actual_access:  read_only
        .address_space:  global
        .offset:         64
        .size:           8
        .value_kind:     global_buffer
      - .address_space:  global
        .offset:         72
        .size:           8
        .value_kind:     global_buffer
      - .actual_access:  read_only
        .address_space:  global
        .offset:         80
        .size:           8
        .value_kind:     global_buffer
      - .actual_access:  write_only
        .address_space:  global
        .offset:         88
        .size:           8
        .value_kind:     global_buffer
    .group_segment_fixed_size: 0
    .kernarg_segment_align: 8
    .kernarg_segment_size: 96
    .language:       OpenCL C
    .language_version:
      - 2
      - 0
    .max_flat_workgroup_size: 512
    .name:           _Z10ffn_kernelPKfS0_PKDF16_S2_S0_S2_S0_S0_S0_S2_S0_Pf
    .private_segment_fixed_size: 0
    .sgpr_count:     24
    .sgpr_spill_count: 0
    .symbol:         _Z10ffn_kernelPKfS0_PKDF16_S2_S0_S2_S0_S0_S0_S2_S0_Pf.kd
    .uniform_work_group_size: 1
    .uses_dynamic_stack: false
    .vgpr_count:     230
    .vgpr_spill_count: 0
    .wavefront_size: 64
